# all five GEMM bodies: non-first units skip accumulator zeroing via a peeled first K-iteration whose first-touch MFMAs take C=0, relaxed vmcnt there; fp8 epilogues drop 6x s_nop 15
# speedup vs baseline: 1.0374x; 1.0374x over previous
.LBB0_178:
	s_mov_b32 s98, 0
	s_mov_b32 s99, 0
	s_cmp_lt_i32 s60, 3
	s_cselect_b64 s[8:9], -1, 0
	v_writelane_b32 v252, s60, 57
	s_and_b64 s[2:3], s[8:9], s[2:3]
	s_andn2_b64 vcc, exec, s[2:3]
	v_writelane_b32 v252, s61, 58
	v_writelane_b32 v252, s56, 59
	s_cbranch_vccnz .LBB0_289
	s_cmpk_gt_i32 s62, 0x7f
	s_cselect_b32 s2, 0xffffffb8, 0
	s_add_i32 s33, s2, s62
	s_mov_b32 s7, 0
	s_cmp_lt_i32 s80, s33
	s_mov_b64 s[2:3], -1
	s_cbranch_scc1 .LBB0_208
	s_load_dwordx4 s[12:15], s[0:1], 0x120
	v_lshlrev_b32_e32 v1, 2, v0
	v_and_b32_e32 v36, 28, v1
	v_mov_b32_e32 v39, 0
	v_cmp_eq_u32_e64 s[2:3], 0, v206
	s_waitcnt lgkmcnt(0)
	s_add_u32 s10, s14, 0x14000
	s_addc_u32 s11, s15, 0
	s_add_u32 s36, s14, 0x12800000
	s_addc_u32 s37, s15, 0
	s_add_u32 s38, s14, 0x2400000
	v_and_b32_e32 v34, 56, v0
	v_mov_b32_e32 v35, v39
	s_addc_u32 s39, s15, 0
	v_lshlrev_b32_e32 v38, 2, v36
	s_mov_b32 s40, 0xc3e00000
	v_mov_b32_e32 v1, 0x43e00000
	s_branch .LBB0_183

.LBB0_223:
	s_and_b64 vcc, exec, s[2:3]
	s_cmp_eq_u32 s98, 0
	s_cbranch_scc1 .Lgk_first_p2b
	v_mov_b32_e32 v141, v135
	v_mov_b32_e32 v139, v135
	s_mov_b32 s27, 0
	s_mov_b64 s[34:35], 0x100
	s_mov_b64 s[36:37], s[22:23]
	ds_read_b128 v[164:167], v149
	ds_read_b128 v[168:171], v149 offset:1024
	ds_read_b128 v[172:175], v149 offset:2048
	ds_read_b128 v[176:179], v149 offset:3072
	ds_read_b128 v[180:183], v150
	ds_read_b128 v[184:187], v150 offset:1024
	ds_read_b128 v[188:191], v150 offset:2048
	ds_read_b128 v[194:197], v150 offset:3072
	s_cmp_eq_u32 s51, s27
	s_cselect_b64 vcc, -1, 0
	s_add_i32 s27, s27, 2
	s_and_b64 s[38:39], vcc, exec
	s_cselect_b32 s38, 0, s34
	s_cselect_b32 s39, 0, s35
	s_add_u32 s38, s14, s38
	s_addc_u32 s39, s15, s39
	s_waitcnt lgkmcnt(0)
	s_add_u32 s66, s30, s34
	s_addc_u32 s67, s31, s35
	s_and_b64 s[64:65], vcc, exec
	v_cndmask_b32_e32 v134, v154, v155, vcc
	v_cndmask_b32_e32 v159, v138, v157, vcc
	v_cndmask_b32_e32 v160, v136, v156, vcc
	s_cselect_b32 s65, s29, s67
	s_cselect_b32 s64, s28, s66
	s_mov_b32 m0, s52
	v_lshl_add_u64 v[232:233], s[36:37], 0, v[138:139]
	ds_read_b128 v[198:201], v151
	ds_read_b128 v[202:205], v151 offset:1024
	ds_read_b128 v[208:211], v151 offset:2048
	ds_read_b128 v[212:215], v151 offset:3072
	ds_read_b128 v[216:219], v151 offset:4096
	ds_read_b128 v[220:223], v151 offset:5120
	ds_read_b128 v[224:227], v151 offset:6144
	ds_read_b128 v[228:231], v151 offset:7168
	global_load_lds_dwordx4 v[232:233], off
	v_lshl_add_u64 v[232:233], s[36:37], 0, v[140:141]
	s_mov_b32 m0, s53
	s_nop 0
	global_load_lds_dwordx4 v[232:233], off
	s_waitcnt vmcnt(24)
	s_waitcnt lgkmcnt(0)
	s_barrier
	s_setprio 1
	s_waitcnt lgkmcnt(0)
	v_mfma_f32_16x16x32_bf16 v[126:129], v[164:167], v[198:201], 0
	v_mfma_f32_16x16x32_bf16 v[122:125], v[172:175], v[198:201], 0
	v_mfma_f32_16x16x32_bf16 v[110:113], v[164:167], v[208:211], 0
	v_mfma_f32_16x16x32_bf16 v[106:109], v[172:175], v[208:211], 0
	v_mfma_f32_16x16x32_bf16 v[94:97], v[164:167], v[216:219], 0
	v_mfma_f32_16x16x32_bf16 v[90:93], v[172:175], v[216:219], 0
	v_mfma_f32_16x16x32_bf16 v[78:81], v[164:167], v[224:227], 0
	v_mfma_f32_16x16x32_bf16 v[74:77], v[172:175], v[224:227], 0
	v_mfma_f32_16x16x32_bf16 v[126:129], v[168:171], v[202:205], v[126:129]
	v_mfma_f32_16x16x32_bf16 v[122:125], v[176:179], v[202:205], v[122:125]
	v_mfma_f32_16x16x32_bf16 v[110:113], v[168:171], v[212:215], v[110:113]
	v_mfma_f32_16x16x32_bf16 v[106:109], v[176:179], v[212:215], v[106:109]
	v_mfma_f32_16x16x32_bf16 v[94:97], v[168:171], v[220:223], v[94:97]
	v_mfma_f32_16x16x32_bf16 v[90:93], v[176:179], v[220:223], v[90:93]
	v_mfma_f32_16x16x32_bf16 v[78:81], v[168:171], v[228:231], v[78:81]
	v_mfma_f32_16x16x32_bf16 v[74:77], v[176:179], v[228:231], v[74:77]
	s_setprio 0
	s_setprio 1
	v_mfma_f32_16x16x32_bf16 v[118:121], v[180:183], v[198:201], 0
	v_mfma_f32_16x16x32_bf16 v[114:117], v[188:191], v[198:201], 0
	v_mfma_f32_16x16x32_bf16 v[102:105], v[180:183], v[208:211], 0
	v_mfma_f32_16x16x32_bf16 v[98:101], v[188:191], v[208:211], 0
	v_mfma_f32_16x16x32_bf16 v[86:89], v[180:183], v[216:219], 0
	v_mfma_f32_16x16x32_bf16 v[82:85], v[188:191], v[216:219], 0
	v_mfma_f32_16x16x32_bf16 v[70:73], v[180:183], v[224:227], 0
	v_mfma_f32_16x16x32_bf16 v[66:69], v[188:191], v[224:227], 0
	v_mfma_f32_16x16x32_bf16 v[118:121], v[184:187], v[202:205], v[118:121]
	v_mfma_f32_16x16x32_bf16 v[114:117], v[194:197], v[202:205], v[114:117]
	v_mfma_f32_16x16x32_bf16 v[102:105], v[184:187], v[212:215], v[102:105]
	v_mfma_f32_16x16x32_bf16 v[98:101], v[194:197], v[212:215], v[98:101]
	v_mfma_f32_16x16x32_bf16 v[86:89], v[184:187], v[220:223], v[86:89]
	v_mfma_f32_16x16x32_bf16 v[82:85], v[194:197], v[220:223], v[82:85]
	v_mfma_f32_16x16x32_bf16 v[70:73], v[184:187], v[228:231], v[70:73]
	v_mfma_f32_16x16x32_bf16 v[66:69], v[194:197], v[228:231], v[66:69]
	s_setprio 0
	s_barrier
	s_mov_b32 m0, s54
	v_lshl_add_u64 v[232:233], s[64:65], 0, v[130:131]
	v_lshl_add_u64 v[234:235], s[64:65], 0, v[132:133]
	s_add_u32 s64, s64, s16
	ds_read_b128 v[198:201], v151 offset:16384
	ds_read_b128 v[202:205], v151 offset:17408
	ds_read_b128 v[208:211], v151 offset:18432
	ds_read_b128 v[212:215], v151 offset:19456
	ds_read_b128 v[216:219], v151 offset:20480
	ds_read_b128 v[220:223], v151 offset:21504
	ds_read_b128 v[224:227], v151 offset:22528
	ds_read_b128 v[228:231], v151 offset:23552
	global_load_lds_dwordx4 v[232:233], off
	s_mov_b32 m0, s55
	s_addc_u32 s65, s65, s17
	global_load_lds_dwordx4 v[234:235], off
	v_lshl_add_u64 v[236:237], s[64:65], 0, v[130:131]
	s_mov_b32 m0, s56
	v_lshl_add_u64 v[238:239], s[64:65], 0, v[132:133]
	global_load_lds_dwordx4 v[236:237], off
	s_mov_b32 m0, s57
	v_mov_b32_e32 v161, v135
	global_load_lds_dwordx4 v[238:239], off
	s_mov_b32 m0, s43
	v_lshl_add_u64 v[240:241], s[38:39], 0, v[134:135]
	global_load_lds_dwordx4 v134, s[38:39]
	s_mov_b32 m0, s44
	s_nop 0
	global_load_lds_dwordx4 v160, s[38:39]
	s_waitcnt vmcnt(24)
	s_waitcnt lgkmcnt(0)
	v_lshl_add_u64 v[160:161], s[38:39], 0, v[160:161]
	s_barrier
	s_setprio 1
	s_waitcnt lgkmcnt(0)
	v_mfma_f32_16x16x32_bf16 v[62:65], v[164:167], v[198:201], 0
	v_mfma_f32_16x16x32_bf16 v[58:61], v[172:175], v[198:201], 0
	v_mfma_f32_16x16x32_bf16 v[46:49], v[164:167], v[208:211], 0
	v_mfma_f32_16x16x32_bf16 v[42:45], v[172:175], v[208:211], 0
	v_mfma_f32_16x16x32_bf16 v[30:33], v[164:167], v[216:219], 0
	v_mfma_f32_16x16x32_bf16 v[26:29], v[172:175], v[216:219], 0
	v_mfma_f32_16x16x32_bf16 v[14:17], v[164:167], v[224:227], 0
	v_mfma_f32_16x16x32_bf16 v[10:13], v[172:175], v[224:227], 0
	v_mfma_f32_16x16x32_bf16 v[62:65], v[168:171], v[202:205], v[62:65]
	v_mfma_f32_16x16x32_bf16 v[58:61], v[176:179], v[202:205], v[58:61]
	v_mfma_f32_16x16x32_bf16 v[46:49], v[168:171], v[212:215], v[46:49]
	v_mfma_f32_16x16x32_bf16 v[42:45], v[176:179], v[212:215], v[42:45]
	v_mfma_f32_16x16x32_bf16 v[30:33], v[168:171], v[220:223], v[30:33]
	v_mfma_f32_16x16x32_bf16 v[26:29], v[176:179], v[220:223], v[26:29]
	v_mfma_f32_16x16x32_bf16 v[14:17], v[168:171], v[228:231], v[14:17]
	v_mfma_f32_16x16x32_bf16 v[10:13], v[176:179], v[228:231], v[10:13]
	s_setprio 0
	s_setprio 1
	v_mfma_f32_16x16x32_bf16 v[54:57], v[180:183], v[198:201], 0
	v_mfma_f32_16x16x32_bf16 v[50:53], v[188:191], v[198:201], 0
	v_mfma_f32_16x16x32_bf16 v[38:41], v[180:183], v[208:211], 0
	v_mfma_f32_16x16x32_bf16 v[34:37], v[188:191], v[208:211], 0
	v_mfma_f32_16x16x32_bf16 v[22:25], v[180:183], v[216:219], 0
	v_mfma_f32_16x16x32_bf16 v[18:21], v[188:191], v[216:219], 0
	v_mfma_f32_16x16x32_bf16 v[6:9], v[180:183], v[224:227], 0
	v_mfma_f32_16x16x32_bf16 v[2:5], v[188:191], v[224:227], 0
	v_mfma_f32_16x16x32_bf16 v[54:57], v[184:187], v[202:205], v[54:57]
	v_mfma_f32_16x16x32_bf16 v[50:53], v[194:197], v[202:205], v[50:53]
	v_mfma_f32_16x16x32_bf16 v[38:41], v[184:187], v[212:215], v[38:41]
	v_mfma_f32_16x16x32_bf16 v[34:37], v[194:197], v[212:215], v[34:37]
	v_mfma_f32_16x16x32_bf16 v[22:25], v[184:187], v[220:223], v[22:25]
	v_mfma_f32_16x16x32_bf16 v[18:21], v[194:197], v[220:223], v[18:21]
	v_mfma_f32_16x16x32_bf16 v[6:9], v[184:187], v[228:231], v[6:9]
	v_mfma_f32_16x16x32_bf16 v[2:5], v[194:197], v[228:231], v[2:5]
	s_setprio 0
	s_barrier
	ds_read_b128 v[164:167], v152
	ds_read_b128 v[168:171], v152 offset:1024
	ds_read_b128 v[172:175], v152 offset:2048
	ds_read_b128 v[176:179], v152 offset:3072
	ds_read_b128 v[180:183], v153
	ds_read_b128 v[184:187], v153 offset:1024
	ds_read_b128 v[188:191], v153 offset:2048
	ds_read_b128 v[194:197], v153 offset:3072
	s_mov_b32 m0, s45
	ds_read_b128 v[198:201], v151 offset:32768
	ds_read_b128 v[202:205], v151 offset:33792
	ds_read_b128 v[208:211], v151 offset:34816
	ds_read_b128 v[212:215], v151 offset:35840
	ds_read_b128 v[216:219], v151 offset:36864
	ds_read_b128 v[220:223], v151 offset:37888
	ds_read_b128 v[224:227], v151 offset:38912
	ds_read_b128 v[228:231], v151 offset:39936
	v_cndmask_b32_e32 v134, v140, v158, vcc
	global_load_lds_dwordx4 v159, s[38:39]
	s_mov_b32 m0, s46
	s_nop 0
	global_load_lds_dwordx4 v134, s[38:39]
	s_waitcnt vmcnt(8)
	s_waitcnt lgkmcnt(0)
	s_barrier
	s_setprio 1
	s_waitcnt lgkmcnt(0)
	v_mfma_f32_16x16x32_bf16 v[126:129], v[164:167], v[198:201], v[126:129]
	v_mfma_f32_16x16x32_bf16 v[122:125], v[172:175], v[198:201], v[122:125]
	v_mfma_f32_16x16x32_bf16 v[110:113], v[164:167], v[208:211], v[110:113]
	v_mfma_f32_16x16x32_bf16 v[106:109], v[172:175], v[208:211], v[106:109]
	v_mfma_f32_16x16x32_bf16 v[94:97], v[164:167], v[216:219], v[94:97]
	v_mfma_f32_16x16x32_bf16 v[90:93], v[172:175], v[216:219], v[90:93]
	v_mfma_f32_16x16x32_bf16 v[78:81], v[164:167], v[224:227], v[78:81]
	v_mfma_f32_16x16x32_bf16 v[74:77], v[172:175], v[224:227], v[74:77]
	v_mfma_f32_16x16x32_bf16 v[126:129], v[168:171], v[202:205], v[126:129]
	v_mfma_f32_16x16x32_bf16 v[122:125], v[176:179], v[202:205], v[122:125]
	v_mfma_f32_16x16x32_bf16 v[110:113], v[168:171], v[212:215], v[110:113]
	v_mfma_f32_16x16x32_bf16 v[106:109], v[176:179], v[212:215], v[106:109]
	v_mfma_f32_16x16x32_bf16 v[94:97], v[168:171], v[220:223], v[94:97]
	v_mfma_f32_16x16x32_bf16 v[90:93], v[176:179], v[220:223], v[90:93]
	v_mfma_f32_16x16x32_bf16 v[78:81], v[168:171], v[228:231], v[78:81]
	v_mfma_f32_16x16x32_bf16 v[74:77], v[176:179], v[228:231], v[74:77]
	s_setprio 0
	s_setprio 1
	v_mfma_f32_16x16x32_bf16 v[118:121], v[180:183], v[198:201], v[118:121]
	v_mfma_f32_16x16x32_bf16 v[114:117], v[188:191], v[198:201], v[114:117]
	v_mfma_f32_16x16x32_bf16 v[102:105], v[180:183], v[208:211], v[102:105]
	v_mfma_f32_16x16x32_bf16 v[98:101], v[188:191], v[208:211], v[98:101]
	v_mfma_f32_16x16x32_bf16 v[86:89], v[180:183], v[216:219], v[86:89]
	v_mfma_f32_16x16x32_bf16 v[82:85], v[188:191], v[216:219], v[82:85]
	v_mfma_f32_16x16x32_bf16 v[70:73], v[180:183], v[224:227], v[70:73]
	v_mfma_f32_16x16x32_bf16 v[66:69], v[188:191], v[224:227], v[66:69]
	v_mfma_f32_16x16x32_bf16 v[118:121], v[184:187], v[202:205], v[118:121]
	v_mfma_f32_16x16x32_bf16 v[114:117], v[194:197], v[202:205], v[114:117]
	v_mfma_f32_16x16x32_bf16 v[102:105], v[184:187], v[212:215], v[102:105]
	v_mfma_f32_16x16x32_bf16 v[98:101], v[194:197], v[212:215], v[98:101]
	v_mfma_f32_16x16x32_bf16 v[86:89], v[184:187], v[220:223], v[86:89]
	v_mfma_f32_16x16x32_bf16 v[82:85], v[194:197], v[220:223], v[82:85]
	v_mfma_f32_16x16x32_bf16 v[70:73], v[184:187], v[228:231], v[70:73]
	v_mfma_f32_16x16x32_bf16 v[66:69], v[194:197], v[228:231], v[66:69]
	s_setprio 0
	s_barrier
	s_mov_b32 m0, s58
	v_lshl_add_u64 v[232:233], v[232:233], 0, s[20:21]
	ds_read_b128 v[198:201], v151 offset:49152
	ds_read_b128 v[202:205], v151 offset:50176
	ds_read_b128 v[208:211], v151 offset:51200
	ds_read_b128 v[212:215], v151 offset:52224
	ds_read_b128 v[216:219], v151 offset:53248
	ds_read_b128 v[220:223], v151 offset:54272
	ds_read_b128 v[224:227], v151 offset:55296
	ds_read_b128 v[228:231], v151 offset:56320
	global_load_lds_dwordx4 v[232:233], off
	v_lshl_add_u64 v[232:233], v[234:235], 0, s[20:21]
	s_mov_b32 m0, s59
	v_lshl_add_u64 v[160:161], v[160:161], 0, s[20:21]
	global_load_lds_dwordx4 v[232:233], off
	v_lshl_add_u64 v[232:233], v[236:237], 0, s[20:21]
	s_mov_b32 m0, s60
	s_nop 0
	global_load_lds_dwordx4 v[232:233], off
	v_lshl_add_u64 v[232:233], v[238:239], 0, s[20:21]
	s_mov_b32 m0, s61
	s_nop 0
	global_load_lds_dwordx4 v[232:233], off
	v_lshl_add_u64 v[232:233], v[240:241], 0, s[20:21]
	s_mov_b32 m0, s49
	s_nop 0
	global_load_lds_dwordx4 v[232:233], off
	s_mov_b32 m0, s50
	s_nop 0
	global_load_lds_dwordx4 v[160:161], off
	s_waitcnt vmcnt(8)
	s_waitcnt lgkmcnt(0)
	s_barrier
	s_setprio 1
	s_waitcnt lgkmcnt(0)
	v_mfma_f32_16x16x32_bf16 v[62:65], v[164:167], v[198:201], v[62:65]
	v_mfma_f32_16x16x32_bf16 v[58:61], v[172:175], v[198:201], v[58:61]
	v_mfma_f32_16x16x32_bf16 v[46:49], v[164:167], v[208:211], v[46:49]
	v_mfma_f32_16x16x32_bf16 v[42:45], v[172:175], v[208:211], v[42:45]
	v_mfma_f32_16x16x32_bf16 v[30:33], v[164:167], v[216:219], v[30:33]
	v_mfma_f32_16x16x32_bf16 v[26:29], v[172:175], v[216:219], v[26:29]
	v_mfma_f32_16x16x32_bf16 v[14:17], v[164:167], v[224:227], v[14:17]
	v_mfma_f32_16x16x32_bf16 v[10:13], v[172:175], v[224:227], v[10:13]
	v_mfma_f32_16x16x32_bf16 v[62:65], v[168:171], v[202:205], v[62:65]
	v_mfma_f32_16x16x32_bf16 v[58:61], v[176:179], v[202:205], v[58:61]
	v_mfma_f32_16x16x32_bf16 v[46:49], v[168:171], v[212:215], v[46:49]
	v_mfma_f32_16x16x32_bf16 v[42:45], v[176:179], v[212:215], v[42:45]
	v_mfma_f32_16x16x32_bf16 v[30:33], v[168:171], v[220:223], v[30:33]
	v_mfma_f32_16x16x32_bf16 v[26:29], v[176:179], v[220:223], v[26:29]
	v_mfma_f32_16x16x32_bf16 v[14:17], v[168:171], v[228:231], v[14:17]
	v_mfma_f32_16x16x32_bf16 v[10:13], v[176:179], v[228:231], v[10:13]
	s_setprio 0
	s_setprio 1
	v_mfma_f32_16x16x32_bf16 v[54:57], v[180:183], v[198:201], v[54:57]
	v_mfma_f32_16x16x32_bf16 v[50:53], v[188:191], v[198:201], v[50:53]
	v_mfma_f32_16x16x32_bf16 v[38:41], v[180:183], v[208:211], v[38:41]
	v_mfma_f32_16x16x32_bf16 v[34:37], v[188:191], v[208:211], v[34:37]
	v_mfma_f32_16x16x32_bf16 v[22:25], v[180:183], v[216:219], v[22:25]
	v_mfma_f32_16x16x32_bf16 v[18:21], v[188:191], v[216:219], v[18:21]
	v_mfma_f32_16x16x32_bf16 v[6:9], v[180:183], v[224:227], v[6:9]
	v_mfma_f32_16x16x32_bf16 v[2:5], v[188:191], v[224:227], v[2:5]
	v_mfma_f32_16x16x32_bf16 v[54:57], v[184:187], v[202:205], v[54:57]
	v_mfma_f32_16x16x32_bf16 v[50:53], v[194:197], v[202:205], v[50:53]
	v_mfma_f32_16x16x32_bf16 v[38:41], v[184:187], v[212:215], v[38:41]
	v_mfma_f32_16x16x32_bf16 v[34:37], v[194:197], v[212:215], v[34:37]
	v_mfma_f32_16x16x32_bf16 v[22:25], v[184:187], v[220:223], v[22:25]
	v_mfma_f32_16x16x32_bf16 v[18:21], v[194:197], v[220:223], v[18:21]
	v_mfma_f32_16x16x32_bf16 v[6:9], v[184:187], v[228:231], v[6:9]
	v_mfma_f32_16x16x32_bf16 v[2:5], v[194:197], v[228:231], v[2:5]
	s_setprio 0
	s_barrier
	s_add_u32 s34, s34, 0x100
	s_addc_u32 s35, s35, 0
	s_add_u32 s36, s36, 0x100
	s_addc_u32 s37, s37, 0
	s_cmp_ge_i32 s27, s47
	s_cbranch_scc1 .LBB0_227
	s_branch .LBB0_225

.LBB0_229:
	v_lshl_or_b32 v156, s12, 8, v148
	v_lshl_add_u32 v134, s48, 8, v137
	v_ashrrev_i32_e32 v157, 31, v156
	v_mov_b64_e32 v[158:159], s[10:11]
	v_mad_i64_i32 v[160:161], s[30:31], v134, s62, v[158:159]
	v_lshlrev_b64 v[156:157], 1, v[156:157]
	v_lshl_add_u64 v[160:161], v[160:161], 0, v[156:157]
	v_cvt_pk_bf16_f32 v126, v126, v127
	v_cvt_pk_bf16_f32 v127, v128, v129
	v_cvt_pk_bf16_f32 v128, v122, v123
	v_cvt_pk_bf16_f32 v129, v124, v125
	global_store_dwordx4 v[160:161], v[126:129], off
	v_cvt_pk_bf16_f32 v118, v118, v119
	v_cvt_pk_bf16_f32 v119, v120, v121
	v_cvt_pk_bf16_f32 v120, v114, v115
	v_or_b32_e32 v114, 16, v134
	v_mad_i64_i32 v[114:115], s[30:31], v114, s62, v[158:159]
	v_lshl_add_u64 v[114:115], v[114:115], 0, v[156:157]
	v_cvt_pk_bf16_f32 v121, v116, v117
	global_store_dwordx4 v[160:161], v[118:121], off offset:64
	v_cvt_pk_bf16_f32 v110, v110, v111
	v_cvt_pk_bf16_f32 v111, v112, v113
	v_cvt_pk_bf16_f32 v112, v106, v107
	v_cvt_pk_bf16_f32 v113, v108, v109
	global_store_dwordx4 v[114:115], v[110:113], off
	v_cvt_pk_bf16_f32 v102, v102, v103
	v_cvt_pk_bf16_f32 v103, v104, v105
	v_cvt_pk_bf16_f32 v104, v98, v99
	v_or_b32_e32 v98, 32, v134
	v_mad_i64_i32 v[98:99], s[30:31], v98, s62, v[158:159]
	v_lshl_add_u64 v[98:99], v[98:99], 0, v[156:157]
	v_cvt_pk_bf16_f32 v105, v100, v101
	global_store_dwordx4 v[114:115], v[102:105], off offset:64
	v_cvt_pk_bf16_f32 v94, v94, v95
	v_cvt_pk_bf16_f32 v95, v96, v97
	v_cvt_pk_bf16_f32 v96, v90, v91
	v_cvt_pk_bf16_f32 v97, v92, v93
	global_store_dwordx4 v[98:99], v[94:97], off
	v_cvt_pk_bf16_f32 v86, v86, v87
	v_cvt_pk_bf16_f32 v87, v88, v89
	v_cvt_pk_bf16_f32 v88, v82, v83
	v_or_b32_e32 v82, 48, v134
	v_mad_i64_i32 v[82:83], s[30:31], v82, s62, v[158:159]
	v_lshl_add_u64 v[82:83], v[82:83], 0, v[156:157]
	v_cvt_pk_bf16_f32 v89, v84, v85
	global_store_dwordx4 v[98:99], v[86:89], off offset:64
	v_cvt_pk_bf16_f32 v78, v78, v79
	v_cvt_pk_bf16_f32 v79, v80, v81
	v_cvt_pk_bf16_f32 v80, v74, v75
	v_cvt_pk_bf16_f32 v81, v76, v77
	global_store_dwordx4 v[82:83], v[78:81], off
	v_cvt_pk_bf16_f32 v70, v70, v71
	v_cvt_pk_bf16_f32 v71, v72, v73
	v_cvt_pk_bf16_f32 v72, v66, v67
	v_add_u32_e32 v66, 0x80, v134
	v_mad_i64_i32 v[66:67], s[30:31], v66, s62, v[158:159]
	v_lshl_add_u64 v[66:67], v[66:67], 0, v[156:157]
	v_cvt_pk_bf16_f32 v73, v68, v69
	global_store_dwordx4 v[82:83], v[70:73], off offset:64
	v_cvt_pk_bf16_f32 v62, v62, v63
	v_cvt_pk_bf16_f32 v63, v64, v65
	v_cvt_pk_bf16_f32 v64, v58, v59
	v_cvt_pk_bf16_f32 v65, v60, v61
	global_store_dwordx4 v[66:67], v[62:65], off
	v_cvt_pk_bf16_f32 v54, v54, v55
	v_cvt_pk_bf16_f32 v55, v56, v57
	v_cvt_pk_bf16_f32 v56, v50, v51
	v_add_u32_e32 v50, 0x90, v134
	v_mad_i64_i32 v[50:51], s[30:31], v50, s62, v[158:159]
	v_lshl_add_u64 v[50:51], v[50:51], 0, v[156:157]
	v_cvt_pk_bf16_f32 v57, v52, v53
	global_store_dwordx4 v[66:67], v[54:57], off offset:64
	v_cvt_pk_bf16_f32 v46, v46, v47
	v_cvt_pk_bf16_f32 v47, v48, v49
	v_cvt_pk_bf16_f32 v48, v42, v43
	v_cvt_pk_bf16_f32 v49, v44, v45
	global_store_dwordx4 v[50:51], v[46:49], off
	v_cvt_pk_bf16_f32 v38, v38, v39
	v_cvt_pk_bf16_f32 v39, v40, v41
	v_cvt_pk_bf16_f32 v40, v34, v35
	v_add_u32_e32 v34, 0xa0, v134
	v_mad_i64_i32 v[34:35], s[30:31], v34, s62, v[158:159]
	v_lshl_add_u64 v[34:35], v[34:35], 0, v[156:157]
	v_cvt_pk_bf16_f32 v41, v36, v37
	global_store_dwordx4 v[50:51], v[38:41], off offset:64
	v_cvt_pk_bf16_f32 v30, v30, v31
	v_cvt_pk_bf16_f32 v31, v32, v33
	v_cvt_pk_bf16_f32 v32, v26, v27
	v_cvt_pk_bf16_f32 v33, v28, v29
	global_store_dwordx4 v[34:35], v[30:33], off
	v_cvt_pk_bf16_f32 v22, v22, v23
	v_cvt_pk_bf16_f32 v23, v24, v25
	v_cvt_pk_bf16_f32 v24, v18, v19
	v_add_u32_e32 v18, 0xb0, v134
	v_mad_i64_i32 v[18:19], s[30:31], v18, s62, v[158:159]
	v_lshl_add_u64 v[18:19], v[18:19], 0, v[156:157]
	s_and_b64 vcc, exec, s[6:7]
	s_mov_b64 s[6:7], -1
	v_cvt_pk_bf16_f32 v25, v20, v21
	global_store_dwordx4 v[34:35], v[22:25], off offset:64
	v_cvt_pk_bf16_f32 v14, v14, v15
	v_cvt_pk_bf16_f32 v15, v16, v17
	v_cvt_pk_bf16_f32 v16, v10, v11
	v_cvt_pk_bf16_f32 v17, v12, v13
	global_store_dwordx4 v[18:19], v[14:17], off
	v_cvt_pk_bf16_f32 v6, v6, v7
	v_cvt_pk_bf16_f32 v7, v8, v9
	v_cvt_pk_bf16_f32 v8, v2, v3
	v_cvt_pk_bf16_f32 v9, v4, v5
	global_store_dwordx4 v[18:19], v[6:9], off offset:64
	s_mov_b32 s98, 1
	s_cbranch_vccnz .LBB0_216
	s_andn2_b64 vcc, exec, s[18:19]
	s_cbranch_vccnz .LBB0_215
	s_barrier
	s_branch .LBB0_215

.LBB0_252:
	s_andn2_b64 vcc, exec, s[22:23]
	s_cmp_eq_u32 s99, 0
	s_cbranch_scc1 .Lgk_first_p2f
	v_mov_b32_e32 v179, v169
	v_mov_b32_e32 v177, v169
	s_mov_b32 s27, 0
	s_mov_b64 s[34:35], 0x100
	s_mov_b64 s[36:37], s[20:21]
	ds_read_b128 v[26:29], v197
	ds_read_b128 v[30:33], v197 offset:1024
	ds_read_b128 v[18:21], v197 offset:2048
	ds_read_b128 v[22:25], v197 offset:3072
	ds_read_b128 v[10:13], v198
	ds_read_b128 v[14:17], v198 offset:1024
	ds_read_b128 v[2:5], v198 offset:2048
	ds_read_b128 v[6:9], v198 offset:3072
	s_cmp_eq_u32 s52, s27
	s_cselect_b64 vcc, -1, 0
	s_add_i32 s27, s27, 2
	s_and_b64 s[38:39], vcc, exec
	s_cselect_b32 s38, 0, s34
	s_cselect_b32 s39, 0, s35
	s_add_u32 s38, s12, s38
	s_addc_u32 s39, s13, s39
	s_waitcnt lgkmcnt(0)
	s_add_u32 s60, s30, s34
	s_addc_u32 s61, s31, s35
	s_and_b64 s[40:41], vcc, exec
	v_cndmask_b32_e32 v168, v200, v201, vcc
	v_cndmask_b32_e32 v205, v176, v203, vcc
	v_cndmask_b32_e32 v188, v174, v202, vcc
	s_cselect_b32 s41, s29, s61
	s_cselect_b32 s40, s28, s60
	v_lshl_add_u64 v[190:191], s[36:37], 0, v[176:177]
	s_add_i32 m0, s45, 0xc000
	ds_read_b128 v[180:183], v199
	ds_read_b128 v[184:187], v199 offset:1024
	ds_read_b128 v[208:211], v199 offset:2048
	ds_read_b128 v[212:215], v199 offset:3072
	ds_read_b128 v[216:219], v199 offset:4096
	ds_read_b128 v[220:223], v199 offset:5120
	ds_read_b128 v[224:227], v199 offset:6144
	ds_read_b128 v[228:231], v199 offset:7168
	global_load_lds_dwordx4 v[190:191], off
	v_lshl_add_u64 v[190:191], s[36:37], 0, v[178:179]
	s_add_i32 m0, s45, 0xe000
	s_nop 0
	global_load_lds_dwordx4 v[190:191], off
	s_waitcnt vmcnt(24)
	s_waitcnt lgkmcnt(0)
	s_barrier
	s_setprio 1
	s_waitcnt lgkmcnt(0)
	v_mfma_scale_f32_16x16x128_f8f6f4 v[158:161], v[26:33], v[180:187], 0, v193, v194 op_sel_hi:[0,0,0]
	v_mfma_scale_f32_16x16x128_f8f6f4 v[154:157], v[18:25], v[180:187], 0, v193, v194 op_sel_hi:[0,0,0]
	v_mfma_scale_f32_16x16x128_f8f6f4 v[142:145], v[26:33], v[208:215], 0, v193, v194 op_sel_hi:[0,0,0]
	v_mfma_scale_f32_16x16x128_f8f6f4 v[138:141], v[18:25], v[208:215], 0, v193, v194 op_sel_hi:[0,0,0]
	v_mfma_scale_f32_16x16x128_f8f6f4 v[126:129], v[26:33], v[216:223], 0, v193, v194 op_sel_hi:[0,0,0]
	v_mfma_scale_f32_16x16x128_f8f6f4 v[122:125], v[18:25], v[216:223], 0, v193, v194 op_sel_hi:[0,0,0]
	v_mfma_scale_f32_16x16x128_f8f6f4 v[110:113], v[26:33], v[224:231], 0, v193, v194 op_sel_hi:[0,0,0]
	v_mfma_scale_f32_16x16x128_f8f6f4 v[106:109], v[18:25], v[224:231], 0, v193, v194 op_sel_hi:[0,0,0]
	s_setprio 0
	s_setprio 1
	v_mfma_scale_f32_16x16x128_f8f6f4 v[150:153], v[10:17], v[180:187], 0, v193, v194 op_sel_hi:[0,0,0]
	v_mfma_scale_f32_16x16x128_f8f6f4 v[146:149], v[2:9], v[180:187], 0, v193, v194 op_sel_hi:[0,0,0]
	v_mfma_scale_f32_16x16x128_f8f6f4 v[134:137], v[10:17], v[208:215], 0, v193, v194 op_sel_hi:[0,0,0]
	v_mfma_scale_f32_16x16x128_f8f6f4 v[130:133], v[2:9], v[208:215], 0, v193, v194 op_sel_hi:[0,0,0]
	v_mfma_scale_f32_16x16x128_f8f6f4 v[118:121], v[10:17], v[216:223], 0, v193, v194 op_sel_hi:[0,0,0]
	v_mfma_scale_f32_16x16x128_f8f6f4 v[114:117], v[2:9], v[216:223], 0, v193, v194 op_sel_hi:[0,0,0]
	v_mfma_scale_f32_16x16x128_f8f6f4 v[102:105], v[10:17], v[224:231], 0, v193, v194 op_sel_hi:[0,0,0]
	v_mfma_scale_f32_16x16x128_f8f6f4 v[98:101], v[2:9], v[224:231], 0, v193, v194 op_sel_hi:[0,0,0]
	s_setprio 0
	s_barrier
	s_add_i32 s60, s55, s44
	v_lshl_add_u64 v[180:181], s[40:41], 0, v[164:165]
	s_mov_b32 m0, s60
	ds_read_b128 v[208:211], v199 offset:16384
	ds_read_b128 v[212:215], v199 offset:17408
	ds_read_b128 v[216:219], v199 offset:18432
	ds_read_b128 v[220:223], v199 offset:19456
	ds_read_b128 v[224:227], v199 offset:20480
	ds_read_b128 v[228:231], v199 offset:21504
	ds_read_b128 v[232:235], v199 offset:22528
	ds_read_b128 v[236:239], v199 offset:23552
	global_load_lds_dwordx4 v[180:181], off
	s_add_i32 m0, s60, 0x2000
	v_lshl_add_u64 v[182:183], s[40:41], 0, v[166:167]
	s_add_u32 s40, s40, s14
	s_addc_u32 s41, s41, s15
	s_add_i32 s60, s56, s44
	global_load_lds_dwordx4 v[182:183], off
	v_lshl_add_u64 v[184:185], s[40:41], 0, v[164:165]
	s_mov_b32 m0, s60
	v_lshl_add_u64 v[186:187], s[40:41], 0, v[166:167]
	global_load_lds_dwordx4 v[184:185], off
	s_add_i32 m0, s60, 0x2000
	v_mov_b32_e32 v189, v169
	global_load_lds_dwordx4 v[186:187], off
	s_mov_b32 m0, s45
	v_lshl_add_u64 v[190:191], s[38:39], 0, v[168:169]
	global_load_lds_dwordx4 v168, s[38:39]
	s_mov_b32 m0, s46
	s_nop 0
	global_load_lds_dwordx4 v188, s[38:39]
	s_waitcnt vmcnt(24)
	s_waitcnt lgkmcnt(0)
	v_lshl_add_u64 v[188:189], s[38:39], 0, v[188:189]
	s_barrier
	s_setprio 1
	s_waitcnt lgkmcnt(0)
	v_mfma_scale_f32_16x16x128_f8f6f4 v[94:97], v[26:33], v[208:215], 0, v193, v194 op_sel_hi:[0,0,0]
	v_mfma_scale_f32_16x16x128_f8f6f4 v[90:93], v[18:25], v[208:215], 0, v193, v194 op_sel_hi:[0,0,0]
	v_mfma_scale_f32_16x16x128_f8f6f4 v[78:81], v[26:33], v[216:223], 0, v193, v194 op_sel_hi:[0,0,0]
	v_mfma_scale_f32_16x16x128_f8f6f4 v[74:77], v[18:25], v[216:223], 0, v193, v194 op_sel_hi:[0,0,0]
	v_mfma_scale_f32_16x16x128_f8f6f4 v[62:65], v[26:33], v[224:231], 0, v193, v194 op_sel_hi:[0,0,0]
	v_mfma_scale_f32_16x16x128_f8f6f4 v[58:61], v[18:25], v[224:231], 0, v193, v194 op_sel_hi:[0,0,0]
	v_mfma_scale_f32_16x16x128_f8f6f4 v[46:49], v[26:33], v[232:239], 0, v193, v194 op_sel_hi:[0,0,0]
	v_mfma_scale_f32_16x16x128_f8f6f4 v[42:45], v[18:25], v[232:239], 0, v193, v194 op_sel_hi:[0,0,0]
	s_setprio 0
	s_setprio 1
	v_mfma_scale_f32_16x16x128_f8f6f4 v[86:89], v[10:17], v[208:215], 0, v193, v194 op_sel_hi:[0,0,0]
	v_mfma_scale_f32_16x16x128_f8f6f4 v[82:85], v[2:9], v[208:215], 0, v193, v194 op_sel_hi:[0,0,0]
	v_mfma_scale_f32_16x16x128_f8f6f4 v[70:73], v[10:17], v[216:223], 0, v193, v194 op_sel_hi:[0,0,0]
	v_mfma_scale_f32_16x16x128_f8f6f4 v[66:69], v[2:9], v[216:223], 0, v193, v194 op_sel_hi:[0,0,0]
	v_mfma_scale_f32_16x16x128_f8f6f4 v[54:57], v[10:17], v[224:231], 0, v193, v194 op_sel_hi:[0,0,0]
	v_mfma_scale_f32_16x16x128_f8f6f4 v[50:53], v[2:9], v[224:231], 0, v193, v194 op_sel_hi:[0,0,0]
	v_mfma_scale_f32_16x16x128_f8f6f4 v[38:41], v[10:17], v[232:239], 0, v193, v194 op_sel_hi:[0,0,0]
	v_mfma_scale_f32_16x16x128_f8f6f4 v[34:37], v[2:9], v[232:239], 0, v193, v194 op_sel_hi:[0,0,0]
	s_setprio 0
	s_barrier
	s_add_i32 s40, 0, 0x18000
	s_add_i32 s41, 0, 0x1c000
	v_add_u32_e32 v2, s40, v195
	v_add_u32_e32 v6, s41, v195
	ds_read_b128 v[26:29], v2
	ds_read_b128 v[30:33], v2 offset:1024
	ds_read_b128 v[18:21], v2 offset:2048
	ds_read_b128 v[22:25], v2 offset:3072
	ds_read_b128 v[10:13], v6
	ds_read_b128 v[14:17], v6 offset:1024
	ds_read_b128 v[2:5], v6 offset:2048
	ds_read_b128 v[6:9], v6 offset:3072
	s_mov_b32 m0, s47
	ds_read_b128 v[208:211], v199 offset:32768
	ds_read_b128 v[212:215], v199 offset:33792
	ds_read_b128 v[216:219], v199 offset:34816
	ds_read_b128 v[220:223], v199 offset:35840
	ds_read_b128 v[224:227], v199 offset:36864
	ds_read_b128 v[228:231], v199 offset:37888
	ds_read_b128 v[232:235], v199 offset:38912
	ds_read_b128 v[236:239], v199 offset:39936
	v_cndmask_b32_e32 v168, v178, v204, vcc
	global_load_lds_dwordx4 v205, s[38:39]
	s_mov_b32 m0, s48
	s_nop 0
	global_load_lds_dwordx4 v168, s[38:39]
	s_waitcnt vmcnt(8)
	s_waitcnt lgkmcnt(0)
	s_barrier
	s_setprio 1
	s_waitcnt lgkmcnt(0)
	v_mfma_scale_f32_16x16x128_f8f6f4 v[158:161], v[26:33], v[208:215], v[158:161], v193, v194 op_sel_hi:[0,0,0]
	v_mfma_scale_f32_16x16x128_f8f6f4 v[154:157], v[18:25], v[208:215], v[154:157], v193, v194 op_sel_hi:[0,0,0]
	v_mfma_scale_f32_16x16x128_f8f6f4 v[142:145], v[26:33], v[216:223], v[142:145], v193, v194 op_sel_hi:[0,0,0]
	v_mfma_scale_f32_16x16x128_f8f6f4 v[138:141], v[18:25], v[216:223], v[138:141], v193, v194 op_sel_hi:[0,0,0]
	v_mfma_scale_f32_16x16x128_f8f6f4 v[126:129], v[26:33], v[224:231], v[126:129], v193, v194 op_sel_hi:[0,0,0]
	v_mfma_scale_f32_16x16x128_f8f6f4 v[122:125], v[18:25], v[224:231], v[122:125], v193, v194 op_sel_hi:[0,0,0]
	v_mfma_scale_f32_16x16x128_f8f6f4 v[110:113], v[26:33], v[232:239], v[110:113], v193, v194 op_sel_hi:[0,0,0]
	v_mfma_scale_f32_16x16x128_f8f6f4 v[106:109], v[18:25], v[232:239], v[106:109], v193, v194 op_sel_hi:[0,0,0]
	s_setprio 0
	s_setprio 1
	v_mfma_scale_f32_16x16x128_f8f6f4 v[150:153], v[10:17], v[208:215], v[150:153], v193, v194 op_sel_hi:[0,0,0]
	v_mfma_scale_f32_16x16x128_f8f6f4 v[146:149], v[2:9], v[208:215], v[146:149], v193, v194 op_sel_hi:[0,0,0]
	v_mfma_scale_f32_16x16x128_f8f6f4 v[134:137], v[10:17], v[216:223], v[134:137], v193, v194 op_sel_hi:[0,0,0]
	v_mfma_scale_f32_16x16x128_f8f6f4 v[130:133], v[2:9], v[216:223], v[130:133], v193, v194 op_sel_hi:[0,0,0]
	v_mfma_scale_f32_16x16x128_f8f6f4 v[118:121], v[10:17], v[224:231], v[118:121], v193, v194 op_sel_hi:[0,0,0]
	v_mfma_scale_f32_16x16x128_f8f6f4 v[114:117], v[2:9], v[224:231], v[114:117], v193, v194 op_sel_hi:[0,0,0]
	v_mfma_scale_f32_16x16x128_f8f6f4 v[102:105], v[10:17], v[232:239], v[102:105], v193, v194 op_sel_hi:[0,0,0]
	v_mfma_scale_f32_16x16x128_f8f6f4 v[98:101], v[2:9], v[232:239], v[98:101], v193, v194 op_sel_hi:[0,0,0]
	s_setprio 0
	s_barrier
	s_add_i32 s38, s40, s44
	v_lshl_add_u64 v[180:181], v[180:181], 0, s[18:19]
	s_mov_b32 m0, s38
	ds_read_b128 v[208:211], v199 offset:49152
	ds_read_b128 v[212:215], v199 offset:50176
	ds_read_b128 v[216:219], v199 offset:51200
	ds_read_b128 v[220:223], v199 offset:52224
	ds_read_b128 v[224:227], v199 offset:53248
	ds_read_b128 v[228:231], v199 offset:54272
	ds_read_b128 v[232:235], v199 offset:55296
	ds_read_b128 v[236:239], v199 offset:56320
	global_load_lds_dwordx4 v[180:181], off
	v_lshl_add_u64 v[180:181], v[182:183], 0, s[18:19]
	s_add_i32 m0, s38, 0x2000
	s_add_i32 s38, s41, s44
	global_load_lds_dwordx4 v[180:181], off
	v_lshl_add_u64 v[180:181], v[184:185], 0, s[18:19]
	s_mov_b32 m0, s38
	s_nop 0
	global_load_lds_dwordx4 v[180:181], off
	v_lshl_add_u64 v[180:181], v[186:187], 0, s[18:19]
	s_add_i32 m0, s38, 0x2000
	s_nop 0
	global_load_lds_dwordx4 v[180:181], off
	v_lshl_add_u64 v[180:181], v[190:191], 0, s[18:19]
	s_mov_b32 m0, s50
	s_nop 0
	global_load_lds_dwordx4 v[180:181], off
	v_lshl_add_u64 v[180:181], v[188:189], 0, s[18:19]
	s_mov_b32 m0, s51
	s_nop 0
	global_load_lds_dwordx4 v[180:181], off
	s_waitcnt vmcnt(8)
	s_waitcnt lgkmcnt(0)
	s_barrier
	s_setprio 1
	s_waitcnt lgkmcnt(0)
	v_mfma_scale_f32_16x16x128_f8f6f4 v[94:97], v[26:33], v[208:215], v[94:97], v193, v194 op_sel_hi:[0,0,0]
	v_mfma_scale_f32_16x16x128_f8f6f4 v[90:93], v[18:25], v[208:215], v[90:93], v193, v194 op_sel_hi:[0,0,0]
	v_mfma_scale_f32_16x16x128_f8f6f4 v[78:81], v[26:33], v[216:223], v[78:81], v193, v194 op_sel_hi:[0,0,0]
	v_mfma_scale_f32_16x16x128_f8f6f4 v[74:77], v[18:25], v[216:223], v[74:77], v193, v194 op_sel_hi:[0,0,0]
	v_mfma_scale_f32_16x16x128_f8f6f4 v[62:65], v[26:33], v[224:231], v[62:65], v193, v194 op_sel_hi:[0,0,0]
	v_mfma_scale_f32_16x16x128_f8f6f4 v[58:61], v[18:25], v[224:231], v[58:61], v193, v194 op_sel_hi:[0,0,0]
	v_mfma_scale_f32_16x16x128_f8f6f4 v[46:49], v[26:33], v[232:239], v[46:49], v193, v194 op_sel_hi:[0,0,0]
	v_mfma_scale_f32_16x16x128_f8f6f4 v[42:45], v[18:25], v[232:239], v[42:45], v193, v194 op_sel_hi:[0,0,0]
	s_setprio 0
	s_setprio 1
	v_mfma_scale_f32_16x16x128_f8f6f4 v[86:89], v[10:17], v[208:215], v[86:89], v193, v194 op_sel_hi:[0,0,0]
	v_mfma_scale_f32_16x16x128_f8f6f4 v[82:85], v[2:9], v[208:215], v[82:85], v193, v194 op_sel_hi:[0,0,0]
	v_mfma_scale_f32_16x16x128_f8f6f4 v[70:73], v[10:17], v[216:223], v[70:73], v193, v194 op_sel_hi:[0,0,0]
	v_mfma_scale_f32_16x16x128_f8f6f4 v[66:69], v[2:9], v[216:223], v[66:69], v193, v194 op_sel_hi:[0,0,0]
	v_mfma_scale_f32_16x16x128_f8f6f4 v[54:57], v[10:17], v[224:231], v[54:57], v193, v194 op_sel_hi:[0,0,0]
	v_mfma_scale_f32_16x16x128_f8f6f4 v[50:53], v[2:9], v[224:231], v[50:53], v193, v194 op_sel_hi:[0,0,0]
	v_mfma_scale_f32_16x16x128_f8f6f4 v[38:41], v[10:17], v[232:239], v[38:41], v193, v194 op_sel_hi:[0,0,0]
	v_mfma_scale_f32_16x16x128_f8f6f4 v[34:37], v[2:9], v[232:239], v[34:37], v193, v194 op_sel_hi:[0,0,0]
	s_setprio 0
	s_barrier
	s_add_u32 s34, s34, 0x100
	s_addc_u32 s35, s35, 0
	s_add_u32 s36, s36, 0x100
	s_addc_u32 s37, s37, 0
	s_cmp_ge_i32 s27, s49
	s_cbranch_scc1 .LBB0_256
	s_branch .LBB0_254

.LBB0_258:
	v_lshl_or_b32 v4, s6, 8, v196
	v_lshl_add_u32 v12, s59, 8, v175
	v_ashrrev_i32_e32 v5, 31, v4
	v_mov_b64_e32 v[2:3], s[10:11]
	v_mad_i64_i32 v[6:7], s[30:31], v12, s57, v[2:3]
	v_lshlrev_b64 v[4:5], 1, v[4:5]
	v_lshl_add_u64 v[10:11], v[6:7], 0, v[4:5]
	v_cvt_pk_bf16_f32 v6, v158, v159
	v_cvt_pk_bf16_f32 v7, v160, v161
	v_cvt_pk_bf16_f32 v8, v154, v155
	v_cvt_pk_bf16_f32 v9, v156, v157
	global_store_dwordx4 v[10:11], v[6:9], off
	s_and_b64 vcc, exec, s[2:3]
	s_mov_b64 s[2:3], -1
	v_cvt_pk_bf16_f32 v6, v150, v151
	v_cvt_pk_bf16_f32 v7, v152, v153
	v_cvt_pk_bf16_f32 v8, v146, v147
	v_cvt_pk_bf16_f32 v9, v148, v149
	global_store_dwordx4 v[10:11], v[6:9], off offset:64
	s_nop 1
	v_or_b32_e32 v6, 16, v12
	v_mad_i64_i32 v[6:7], s[30:31], v6, s57, v[2:3]
	v_lshl_add_u64 v[10:11], v[6:7], 0, v[4:5]
	v_cvt_pk_bf16_f32 v6, v142, v143
	v_cvt_pk_bf16_f32 v7, v144, v145
	v_cvt_pk_bf16_f32 v8, v138, v139
	v_cvt_pk_bf16_f32 v9, v140, v141
	global_store_dwordx4 v[10:11], v[6:9], off
	s_nop 1
	v_cvt_pk_bf16_f32 v6, v134, v135
	v_cvt_pk_bf16_f32 v7, v136, v137
	v_cvt_pk_bf16_f32 v8, v130, v131
	v_cvt_pk_bf16_f32 v9, v132, v133
	global_store_dwordx4 v[10:11], v[6:9], off offset:64
	s_nop 1
	v_or_b32_e32 v6, 32, v12
	v_mad_i64_i32 v[6:7], s[30:31], v6, s57, v[2:3]
	v_lshl_add_u64 v[10:11], v[6:7], 0, v[4:5]
	v_cvt_pk_bf16_f32 v6, v126, v127
	v_cvt_pk_bf16_f32 v7, v128, v129
	v_cvt_pk_bf16_f32 v8, v122, v123
	v_cvt_pk_bf16_f32 v9, v124, v125
	global_store_dwordx4 v[10:11], v[6:9], off
	s_nop 1
	v_cvt_pk_bf16_f32 v6, v118, v119
	v_cvt_pk_bf16_f32 v7, v120, v121
	v_cvt_pk_bf16_f32 v8, v114, v115
	v_cvt_pk_bf16_f32 v9, v116, v117
	global_store_dwordx4 v[10:11], v[6:9], off offset:64
	s_nop 1
	v_or_b32_e32 v6, 48, v12
	v_mad_i64_i32 v[6:7], s[30:31], v6, s57, v[2:3]
	v_lshl_add_u64 v[10:11], v[6:7], 0, v[4:5]
	v_cvt_pk_bf16_f32 v6, v110, v111
	v_cvt_pk_bf16_f32 v7, v112, v113
	v_cvt_pk_bf16_f32 v8, v106, v107
	v_cvt_pk_bf16_f32 v9, v108, v109
	global_store_dwordx4 v[10:11], v[6:9], off
	s_nop 1
	v_cvt_pk_bf16_f32 v6, v102, v103
	v_cvt_pk_bf16_f32 v7, v104, v105
	v_cvt_pk_bf16_f32 v8, v98, v99
	v_cvt_pk_bf16_f32 v9, v100, v101
	global_store_dwordx4 v[10:11], v[6:9], off offset:64
	s_nop 1
	v_add_u32_e32 v6, 0x80, v12
	v_mad_i64_i32 v[6:7], s[30:31], v6, s57, v[2:3]
	v_lshl_add_u64 v[10:11], v[6:7], 0, v[4:5]
	v_cvt_pk_bf16_f32 v6, v94, v95
	v_cvt_pk_bf16_f32 v7, v96, v97
	v_cvt_pk_bf16_f32 v8, v90, v91
	v_cvt_pk_bf16_f32 v9, v92, v93
	global_store_dwordx4 v[10:11], v[6:9], off
	s_nop 1
	v_cvt_pk_bf16_f32 v6, v86, v87
	v_cvt_pk_bf16_f32 v7, v88, v89
	v_cvt_pk_bf16_f32 v8, v82, v83
	v_cvt_pk_bf16_f32 v9, v84, v85
	global_store_dwordx4 v[10:11], v[6:9], off offset:64
	s_nop 1
	v_add_u32_e32 v6, 0x90, v12
	v_mad_i64_i32 v[6:7], s[30:31], v6, s57, v[2:3]
	v_lshl_add_u64 v[10:11], v[6:7], 0, v[4:5]
	v_cvt_pk_bf16_f32 v6, v78, v79
	v_cvt_pk_bf16_f32 v7, v80, v81
	v_cvt_pk_bf16_f32 v8, v74, v75
	v_cvt_pk_bf16_f32 v9, v76, v77
	global_store_dwordx4 v[10:11], v[6:9], off
	s_nop 1
	v_cvt_pk_bf16_f32 v6, v70, v71
	v_cvt_pk_bf16_f32 v7, v72, v73
	v_cvt_pk_bf16_f32 v8, v66, v67
	v_cvt_pk_bf16_f32 v9, v68, v69
	global_store_dwordx4 v[10:11], v[6:9], off offset:64
	s_nop 1
	v_add_u32_e32 v6, 0xa0, v12
	v_mad_i64_i32 v[6:7], s[30:31], v6, s57, v[2:3]
	v_lshl_add_u64 v[10:11], v[6:7], 0, v[4:5]
	v_cvt_pk_bf16_f32 v6, v62, v63
	v_cvt_pk_bf16_f32 v7, v64, v65
	v_cvt_pk_bf16_f32 v8, v58, v59
	v_cvt_pk_bf16_f32 v9, v60, v61
	global_store_dwordx4 v[10:11], v[6:9], off
	s_nop 1
	v_cvt_pk_bf16_f32 v6, v54, v55
	v_cvt_pk_bf16_f32 v7, v56, v57
	v_cvt_pk_bf16_f32 v8, v50, v51
	v_cvt_pk_bf16_f32 v9, v52, v53
	global_store_dwordx4 v[10:11], v[6:9], off offset:64
	s_nop 1
	v_add_u32_e32 v6, 0xb0, v12
	v_mad_i64_i32 v[2:3], s[30:31], v6, s57, v[2:3]
	v_lshl_add_u64 v[6:7], v[2:3], 0, v[4:5]
	v_cvt_pk_bf16_f32 v2, v46, v47
	v_cvt_pk_bf16_f32 v3, v48, v49
	v_cvt_pk_bf16_f32 v4, v42, v43
	v_cvt_pk_bf16_f32 v5, v44, v45
	global_store_dwordx4 v[6:7], v[2:5], off
	s_nop 1
	v_cvt_pk_bf16_f32 v2, v38, v39
	v_cvt_pk_bf16_f32 v3, v40, v41
	v_cvt_pk_bf16_f32 v4, v34, v35
	v_cvt_pk_bf16_f32 v5, v36, v37
	global_store_dwordx4 v[6:7], v[2:5], off offset:64
	s_mov_b32 s99, 1
	s_cbranch_vccnz .LBB0_244
	s_andn2_b64 vcc, exec, s[16:17]
	s_cbranch_vccnz .LBB0_243
	s_barrier
	s_branch .LBB0_243

.LBB0_1052:
	s_mov_b32 s100, 0
	s_cmp_lt_i32 s60, 7
	s_cselect_b64 s[4:5], -1, 0
	s_and_b64 s[0:1], s[4:5], s[0:1]
	s_andn2_b64 vcc, exec, s[0:1]
	s_mov_b32 s96, s62
	s_cbranch_vccnz .LBB0_1081
	s_movk_i32 s0, 0x1000
	s_cmpk_gt_i32 s92, 0x1ff
	v_readfirstlane_b32 s22, v0
	s_cbranch_scc1 .LBB0_1081
	s_ashr_i32 s33, s92, 31
	s_lshr_b32 s1, s33, 29
	s_add_i32 s6, s92, s1
	s_and_b32 s1, s6, -8
	s_sub_i32 s1, s92, s1
	s_cmp_gt_i32 s1, -1
	s_cbranch_scc0 .LBB0_1056
	s_lshl_b32 s10, s1, 6
	s_mov_b64 s[2:3], 0
	s_branch .LBB0_1057

.LBB0_1072:
	s_andn2_b64 vcc, exec, s[20:21]
	s_cmp_eq_u32 s100, 0
	s_cbranch_scc1 .Lgk_first_p6
	v_mov_b32_e32 v163, v153
	v_mov_b32_e32 v161, v153
	s_mov_b32 s35, 0
	s_mov_b64 s[38:39], 0x100
	s_mov_b64 s[40:41], s[18:19]
	ds_read_b128 v[134:137], v168
	ds_read_b128 v[138:141], v168 offset:1024
	ds_read_b128 v[142:145], v168 offset:2048
	ds_read_b128 v[172:175], v168 offset:3072
	ds_read_b128 v[176:179], v169
	ds_read_b128 v[180:183], v169 offset:1024
	ds_read_b128 v[184:187], v169 offset:2048
	ds_read_b128 v[188:191], v169 offset:3072
	s_cmp_eq_u32 s55, s35
	s_cselect_b64 vcc, -1, 0
	s_add_i32 s35, s35, 2
	s_and_b64 s[42:43], vcc, exec
	s_cselect_b32 s42, 0, s38
	s_cselect_b32 s43, 0, s39
	s_add_u32 s42, s6, s42
	s_addc_u32 s43, s7, s43
	s_add_u32 s68, s36, s38
	s_addc_u32 s69, s37, s39
	s_and_b64 s[66:67], vcc, exec
	v_cndmask_b32_e32 v152, v171, v130, vcc
	v_cndmask_b32_e32 v207, v160, v132, vcc
	v_cndmask_b32_e32 v164, v158, v131, vcc
	s_cselect_b32 s67, s3, s69
	s_cselect_b32 s66, s2, s68
	v_lshl_add_u64 v[204:205], s[40:41], 0, v[160:161]
	s_add_i32 m0, s47, 0xc000
	ds_read_b128 v[192:195], v170
	ds_read_b128 v[196:199], v170 offset:1024
	ds_read_b128 v[200:203], v170 offset:2048
	ds_read_b128 v[208:211], v170 offset:3072
	ds_read_b128 v[212:215], v170 offset:4096
	ds_read_b128 v[216:219], v170 offset:5120
	ds_read_b128 v[220:223], v170 offset:6144
	ds_read_b128 v[224:227], v170 offset:7168
	global_load_lds_dwordx4 v[204:205], off
	v_lshl_add_u64 v[204:205], s[40:41], 0, v[162:163]
	s_add_i32 m0, s47, 0xe000
	s_nop 0
	global_load_lds_dwordx4 v[204:205], off
	s_waitcnt vmcnt(28)
	s_waitcnt lgkmcnt(0)
	s_barrier
	s_setprio 1
	s_waitcnt lgkmcnt(0)
	v_mfma_f32_16x16x32_bf16 v[122:125], v[134:137], v[192:195], 0
	v_mfma_f32_16x16x32_bf16 v[126:129], v[142:145], v[192:195], 0
	v_mfma_f32_16x16x32_bf16 v[110:113], v[134:137], v[200:203], 0
	v_mfma_f32_16x16x32_bf16 v[106:109], v[142:145], v[200:203], 0
	v_mfma_f32_16x16x32_bf16 v[94:97], v[134:137], v[212:215], 0
	v_mfma_f32_16x16x32_bf16 v[90:93], v[142:145], v[212:215], 0
	v_mfma_f32_16x16x32_bf16 v[78:81], v[134:137], v[220:223], 0
	v_mfma_f32_16x16x32_bf16 v[74:77], v[142:145], v[220:223], 0
	v_mfma_f32_16x16x32_bf16 v[122:125], v[138:141], v[196:199], v[122:125]
	v_mfma_f32_16x16x32_bf16 v[126:129], v[172:175], v[196:199], v[126:129]
	v_mfma_f32_16x16x32_bf16 v[110:113], v[138:141], v[208:211], v[110:113]
	v_mfma_f32_16x16x32_bf16 v[106:109], v[172:175], v[208:211], v[106:109]
	v_mfma_f32_16x16x32_bf16 v[94:97], v[138:141], v[216:219], v[94:97]
	v_mfma_f32_16x16x32_bf16 v[90:93], v[172:175], v[216:219], v[90:93]
	v_mfma_f32_16x16x32_bf16 v[78:81], v[138:141], v[224:227], v[78:81]
	v_mfma_f32_16x16x32_bf16 v[74:77], v[172:175], v[224:227], v[74:77]
	s_setprio 0
	s_setprio 1
	v_mfma_f32_16x16x32_bf16 v[118:121], v[176:179], v[192:195], 0
	v_mfma_f32_16x16x32_bf16 v[114:117], v[184:187], v[192:195], 0
	v_mfma_f32_16x16x32_bf16 v[102:105], v[176:179], v[200:203], 0
	v_mfma_f32_16x16x32_bf16 v[98:101], v[184:187], v[200:203], 0
	v_mfma_f32_16x16x32_bf16 v[86:89], v[176:179], v[212:215], 0
	v_mfma_f32_16x16x32_bf16 v[82:85], v[184:187], v[212:215], 0
	v_mfma_f32_16x16x32_bf16 v[70:73], v[176:179], v[220:223], 0
	v_mfma_f32_16x16x32_bf16 v[66:69], v[184:187], v[220:223], 0
	v_mfma_f32_16x16x32_bf16 v[118:121], v[180:183], v[196:199], v[118:121]
	v_mfma_f32_16x16x32_bf16 v[114:117], v[188:191], v[196:199], v[114:117]
	v_mfma_f32_16x16x32_bf16 v[102:105], v[180:183], v[208:211], v[102:105]
	v_mfma_f32_16x16x32_bf16 v[98:101], v[188:191], v[208:211], v[98:101]
	v_mfma_f32_16x16x32_bf16 v[86:89], v[180:183], v[216:219], v[86:89]
	v_mfma_f32_16x16x32_bf16 v[82:85], v[188:191], v[216:219], v[82:85]
	v_mfma_f32_16x16x32_bf16 v[70:73], v[180:183], v[224:227], v[70:73]
	v_mfma_f32_16x16x32_bf16 v[66:69], v[188:191], v[224:227], v[66:69]
	s_setprio 0
	s_barrier
	s_add_i32 s68, s57, s46
	v_lshl_add_u64 v[204:205], s[66:67], 0, v[148:149]
	s_mov_b32 m0, s68
	ds_read_b128 v[192:195], v170 offset:16384
	ds_read_b128 v[196:199], v170 offset:17408
	ds_read_b128 v[200:203], v170 offset:18432
	ds_read_b128 v[208:211], v170 offset:19456
	ds_read_b128 v[212:215], v170 offset:20480
	ds_read_b128 v[216:219], v170 offset:21504
	ds_read_b128 v[220:223], v170 offset:22528
	ds_read_b128 v[224:227], v170 offset:23552
	global_load_lds_dwordx4 v[204:205], off
	s_add_i32 m0, s68, 0x2000
	v_lshl_add_u64 v[228:229], s[66:67], 0, v[150:151]
	s_add_u32 s66, s66, s8
	s_addc_u32 s67, s67, s9
	s_add_i32 s68, s58, s46
	global_load_lds_dwordx4 v[228:229], off
	v_lshl_add_u64 v[230:231], s[66:67], 0, v[148:149]
	s_mov_b32 m0, s68
	v_lshl_add_u64 v[232:233], s[66:67], 0, v[150:151]
	global_load_lds_dwordx4 v[230:231], off
	s_add_i32 m0, s68, 0x2000
	v_mov_b32_e32 v165, v153
	global_load_lds_dwordx4 v[232:233], off
	s_mov_b32 m0, s47
	v_lshl_add_u64 v[234:235], s[42:43], 0, v[152:153]
	global_load_lds_dwordx4 v152, s[42:43]
	s_mov_b32 m0, s48
	s_nop 0
	global_load_lds_dwordx4 v164, s[42:43]
	s_waitcnt vmcnt(28)
	s_waitcnt lgkmcnt(0)
	v_lshl_add_u64 v[164:165], s[42:43], 0, v[164:165]
	s_barrier
	s_setprio 1
	s_waitcnt lgkmcnt(0)
	v_mfma_f32_16x16x32_bf16 v[62:65], v[134:137], v[192:195], 0
	v_mfma_f32_16x16x32_bf16 v[58:61], v[142:145], v[192:195], 0
	v_mfma_f32_16x16x32_bf16 v[46:49], v[134:137], v[200:203], 0
	v_mfma_f32_16x16x32_bf16 v[42:45], v[142:145], v[200:203], 0
	v_mfma_f32_16x16x32_bf16 v[30:33], v[134:137], v[212:215], 0
	v_mfma_f32_16x16x32_bf16 v[26:29], v[142:145], v[212:215], 0
	v_mfma_f32_16x16x32_bf16 v[14:17], v[134:137], v[220:223], 0
	v_mfma_f32_16x16x32_bf16 v[10:13], v[142:145], v[220:223], 0
	v_mfma_f32_16x16x32_bf16 v[62:65], v[138:141], v[196:199], v[62:65]
	v_mfma_f32_16x16x32_bf16 v[58:61], v[172:175], v[196:199], v[58:61]
	v_mfma_f32_16x16x32_bf16 v[46:49], v[138:141], v[208:211], v[46:49]
	v_mfma_f32_16x16x32_bf16 v[42:45], v[172:175], v[208:211], v[42:45]
	v_mfma_f32_16x16x32_bf16 v[30:33], v[138:141], v[216:219], v[30:33]
	v_mfma_f32_16x16x32_bf16 v[26:29], v[172:175], v[216:219], v[26:29]
	v_mfma_f32_16x16x32_bf16 v[14:17], v[138:141], v[224:227], v[14:17]
	v_mfma_f32_16x16x32_bf16 v[10:13], v[172:175], v[224:227], v[10:13]
	s_setprio 0
	s_setprio 1
	v_mfma_f32_16x16x32_bf16 v[54:57], v[176:179], v[192:195], 0
	v_mfma_f32_16x16x32_bf16 v[50:53], v[184:187], v[192:195], 0
	v_mfma_f32_16x16x32_bf16 v[38:41], v[176:179], v[200:203], 0
	v_mfma_f32_16x16x32_bf16 v[34:37], v[184:187], v[200:203], 0
	v_mfma_f32_16x16x32_bf16 v[22:25], v[176:179], v[212:215], 0
	v_mfma_f32_16x16x32_bf16 v[18:21], v[184:187], v[212:215], 0
	v_mfma_f32_16x16x32_bf16 v[6:9], v[176:179], v[220:223], 0
	v_mfma_f32_16x16x32_bf16 v[2:5], v[184:187], v[220:223], 0
	v_mfma_f32_16x16x32_bf16 v[54:57], v[180:183], v[196:199], v[54:57]
	v_mfma_f32_16x16x32_bf16 v[50:53], v[188:191], v[196:199], v[50:53]
	v_mfma_f32_16x16x32_bf16 v[38:41], v[180:183], v[208:211], v[38:41]
	v_mfma_f32_16x16x32_bf16 v[34:37], v[188:191], v[208:211], v[34:37]
	v_mfma_f32_16x16x32_bf16 v[22:25], v[180:183], v[216:219], v[22:25]
	v_mfma_f32_16x16x32_bf16 v[18:21], v[188:191], v[216:219], v[18:21]
	v_mfma_f32_16x16x32_bf16 v[6:9], v[180:183], v[224:227], v[6:9]
	v_mfma_f32_16x16x32_bf16 v[2:5], v[188:191], v[224:227], v[2:5]
	s_setprio 0
	s_barrier
	s_add_i32 s66, 0, 0x18000
	v_add_u32_e32 v152, s66, v166
	s_add_i32 s67, 0, 0x1c000
	ds_read_b128 v[134:137], v152
	ds_read_b128 v[138:141], v152 offset:1024
	ds_read_b128 v[142:145], v152 offset:2048
	ds_read_b128 v[172:175], v152 offset:3072
	v_add_u32_e32 v152, s67, v166
	ds_read_b128 v[176:179], v152
	ds_read_b128 v[180:183], v152 offset:1024
	ds_read_b128 v[184:187], v152 offset:2048
	ds_read_b128 v[188:191], v152 offset:3072
	s_mov_b32 m0, s49
	ds_read_b128 v[192:195], v170 offset:32768
	ds_read_b128 v[196:199], v170 offset:33792
	ds_read_b128 v[200:203], v170 offset:34816
	ds_read_b128 v[208:211], v170 offset:35840
	ds_read_b128 v[212:215], v170 offset:36864
	ds_read_b128 v[216:219], v170 offset:37888
	ds_read_b128 v[220:223], v170 offset:38912
	ds_read_b128 v[224:227], v170 offset:39936
	v_cndmask_b32_e32 v152, v162, v133, vcc
	global_load_lds_dwordx4 v207, s[42:43]
	s_mov_b32 m0, s50
	s_nop 0
	global_load_lds_dwordx4 v152, s[42:43]
	s_waitcnt vmcnt(8)
	s_waitcnt lgkmcnt(0)
	s_barrier
	s_setprio 1
	s_waitcnt lgkmcnt(0)
	v_mfma_f32_16x16x32_bf16 v[122:125], v[134:137], v[192:195], v[122:125]
	v_mfma_f32_16x16x32_bf16 v[126:129], v[142:145], v[192:195], v[126:129]
	v_mfma_f32_16x16x32_bf16 v[110:113], v[134:137], v[200:203], v[110:113]
	v_mfma_f32_16x16x32_bf16 v[106:109], v[142:145], v[200:203], v[106:109]
	v_mfma_f32_16x16x32_bf16 v[94:97], v[134:137], v[212:215], v[94:97]
	v_mfma_f32_16x16x32_bf16 v[90:93], v[142:145], v[212:215], v[90:93]
	v_mfma_f32_16x16x32_bf16 v[78:81], v[134:137], v[220:223], v[78:81]
	v_mfma_f32_16x16x32_bf16 v[74:77], v[142:145], v[220:223], v[74:77]
	v_mfma_f32_16x16x32_bf16 v[122:125], v[138:141], v[196:199], v[122:125]
	v_mfma_f32_16x16x32_bf16 v[126:129], v[172:175], v[196:199], v[126:129]
	v_mfma_f32_16x16x32_bf16 v[110:113], v[138:141], v[208:211], v[110:113]
	v_mfma_f32_16x16x32_bf16 v[106:109], v[172:175], v[208:211], v[106:109]
	v_mfma_f32_16x16x32_bf16 v[94:97], v[138:141], v[216:219], v[94:97]
	v_mfma_f32_16x16x32_bf16 v[90:93], v[172:175], v[216:219], v[90:93]
	v_mfma_f32_16x16x32_bf16 v[78:81], v[138:141], v[224:227], v[78:81]
	v_mfma_f32_16x16x32_bf16 v[74:77], v[172:175], v[224:227], v[74:77]
	s_setprio 0
	s_setprio 1
	v_mfma_f32_16x16x32_bf16 v[118:121], v[176:179], v[192:195], v[118:121]
	v_mfma_f32_16x16x32_bf16 v[114:117], v[184:187], v[192:195], v[114:117]
	v_mfma_f32_16x16x32_bf16 v[102:105], v[176:179], v[200:203], v[102:105]
	v_mfma_f32_16x16x32_bf16 v[98:101], v[184:187], v[200:203], v[98:101]
	v_mfma_f32_16x16x32_bf16 v[86:89], v[176:179], v[212:215], v[86:89]
	v_mfma_f32_16x16x32_bf16 v[82:85], v[184:187], v[212:215], v[82:85]
	v_mfma_f32_16x16x32_bf16 v[70:73], v[176:179], v[220:223], v[70:73]
	v_mfma_f32_16x16x32_bf16 v[66:69], v[184:187], v[220:223], v[66:69]
	v_mfma_f32_16x16x32_bf16 v[118:121], v[180:183], v[196:199], v[118:121]
	v_mfma_f32_16x16x32_bf16 v[114:117], v[188:191], v[196:199], v[114:117]
	v_mfma_f32_16x16x32_bf16 v[102:105], v[180:183], v[208:211], v[102:105]
	v_mfma_f32_16x16x32_bf16 v[98:101], v[188:191], v[208:211], v[98:101]
	v_mfma_f32_16x16x32_bf16 v[86:89], v[180:183], v[216:219], v[86:89]
	v_mfma_f32_16x16x32_bf16 v[82:85], v[188:191], v[216:219], v[82:85]
	v_mfma_f32_16x16x32_bf16 v[70:73], v[180:183], v[224:227], v[70:73]
	v_mfma_f32_16x16x32_bf16 v[66:69], v[188:191], v[224:227], v[66:69]
	s_setprio 0
	s_barrier
	s_add_i32 s42, s66, s46
	v_lshl_add_u64 v[204:205], v[204:205], 0, s[16:17]
	s_mov_b32 m0, s42
	ds_read_b128 v[192:195], v170 offset:49152
	ds_read_b128 v[196:199], v170 offset:50176
	ds_read_b128 v[200:203], v170 offset:51200
	ds_read_b128 v[208:211], v170 offset:52224
	ds_read_b128 v[212:215], v170 offset:53248
	ds_read_b128 v[216:219], v170 offset:54272
	ds_read_b128 v[220:223], v170 offset:55296
	ds_read_b128 v[224:227], v170 offset:56320
	global_load_lds_dwordx4 v[204:205], off
	v_lshl_add_u64 v[204:205], v[228:229], 0, s[16:17]
	s_add_i32 m0, s42, 0x2000
	s_add_i32 s42, s67, s46
	global_load_lds_dwordx4 v[204:205], off
	v_lshl_add_u64 v[204:205], v[230:231], 0, s[16:17]
	s_mov_b32 m0, s42
	v_lshl_add_u64 v[164:165], v[164:165], 0, s[16:17]
	global_load_lds_dwordx4 v[204:205], off
	v_lshl_add_u64 v[204:205], v[232:233], 0, s[16:17]
	s_add_i32 m0, s42, 0x2000
	s_nop 0
	global_load_lds_dwordx4 v[204:205], off
	v_lshl_add_u64 v[204:205], v[234:235], 0, s[16:17]
	s_mov_b32 m0, s53
	s_nop 0
	global_load_lds_dwordx4 v[204:205], off
	s_mov_b32 m0, s54
	s_nop 0
	global_load_lds_dwordx4 v[164:165], off
	s_waitcnt vmcnt(8)
	s_waitcnt lgkmcnt(0)
	s_barrier
	s_setprio 1
	s_waitcnt lgkmcnt(0)
	v_mfma_f32_16x16x32_bf16 v[62:65], v[134:137], v[192:195], v[62:65]
	v_mfma_f32_16x16x32_bf16 v[58:61], v[142:145], v[192:195], v[58:61]
	v_mfma_f32_16x16x32_bf16 v[46:49], v[134:137], v[200:203], v[46:49]
	v_mfma_f32_16x16x32_bf16 v[42:45], v[142:145], v[200:203], v[42:45]
	v_mfma_f32_16x16x32_bf16 v[30:33], v[134:137], v[212:215], v[30:33]
	v_mfma_f32_16x16x32_bf16 v[26:29], v[142:145], v[212:215], v[26:29]
	v_mfma_f32_16x16x32_bf16 v[14:17], v[134:137], v[220:223], v[14:17]
	v_mfma_f32_16x16x32_bf16 v[10:13], v[142:145], v[220:223], v[10:13]
	v_mfma_f32_16x16x32_bf16 v[62:65], v[138:141], v[196:199], v[62:65]
	v_mfma_f32_16x16x32_bf16 v[58:61], v[172:175], v[196:199], v[58:61]
	v_mfma_f32_16x16x32_bf16 v[46:49], v[138:141], v[208:211], v[46:49]
	v_mfma_f32_16x16x32_bf16 v[42:45], v[172:175], v[208:211], v[42:45]
	v_mfma_f32_16x16x32_bf16 v[30:33], v[138:141], v[216:219], v[30:33]
	v_mfma_f32_16x16x32_bf16 v[26:29], v[172:175], v[216:219], v[26:29]
	v_mfma_f32_16x16x32_bf16 v[14:17], v[138:141], v[224:227], v[14:17]
	v_mfma_f32_16x16x32_bf16 v[10:13], v[172:175], v[224:227], v[10:13]
	s_setprio 0
	s_setprio 1
	v_mfma_f32_16x16x32_bf16 v[54:57], v[176:179], v[192:195], v[54:57]
	v_mfma_f32_16x16x32_bf16 v[50:53], v[184:187], v[192:195], v[50:53]
	v_mfma_f32_16x16x32_bf16 v[38:41], v[176:179], v[200:203], v[38:41]
	v_mfma_f32_16x16x32_bf16 v[34:37], v[184:187], v[200:203], v[34:37]
	v_mfma_f32_16x16x32_bf16 v[22:25], v[176:179], v[212:215], v[22:25]
	v_mfma_f32_16x16x32_bf16 v[18:21], v[184:187], v[212:215], v[18:21]
	v_mfma_f32_16x16x32_bf16 v[6:9], v[176:179], v[220:223], v[6:9]
	v_mfma_f32_16x16x32_bf16 v[2:5], v[184:187], v[220:223], v[2:5]
	v_mfma_f32_16x16x32_bf16 v[54:57], v[180:183], v[196:199], v[54:57]
	v_mfma_f32_16x16x32_bf16 v[50:53], v[188:191], v[196:199], v[50:53]
	v_mfma_f32_16x16x32_bf16 v[38:41], v[180:183], v[208:211], v[38:41]
	v_mfma_f32_16x16x32_bf16 v[34:37], v[188:191], v[208:211], v[34:37]
	v_mfma_f32_16x16x32_bf16 v[22:25], v[180:183], v[216:219], v[22:25]
	v_mfma_f32_16x16x32_bf16 v[18:21], v[188:191], v[216:219], v[18:21]
	v_mfma_f32_16x16x32_bf16 v[6:9], v[180:183], v[224:227], v[6:9]
	v_mfma_f32_16x16x32_bf16 v[2:5], v[188:191], v[224:227], v[2:5]
	s_setprio 0
	s_barrier
	s_add_u32 s38, s38, 0x100
	s_addc_u32 s39, s39, 0
	s_add_u32 s40, s40, 0x100
	s_addc_u32 s41, s41, 0
	s_cmp_ge_i32 s35, s52
	s_cbranch_scc1 .LBB0_1075
	s_branch .LBB0_1074

.LBB0_1077:
	v_lshl_or_b32 v164, s65, 8, v167
	v_ashrrev_i32_e32 v165, 31, v164
	v_lshl_add_u64 v[130:131], v[164:165], 2, s[14:15]
	global_load_dwordx4 v[142:145], v[130:131], off
	global_load_dwordx4 v[138:141], v[130:131], off offset:16
	global_load_dwordx4 v[134:137], v[130:131], off offset:128
	s_nop 0
	global_load_dwordx4 v[130:133], v[130:131], off offset:144
	v_lshl_add_u32 v172, s64, 8, v159
	v_ashrrev_i32_e32 v173, 31, v172
	v_or_b32_e32 v174, 16, v172
	v_or_b32_e32 v176, 32, v172
	v_or_b32_e32 v178, 48, v172
	v_lshlrev_b64 v[172:173], 12, v[172:173]
	v_ashrrev_i32_e32 v175, 31, v174
	v_ashrrev_i32_e32 v177, 31, v176
	v_ashrrev_i32_e32 v179, 31, v178
	v_lshlrev_b64 v[180:181], 1, v[164:165]
	v_lshl_add_u64 v[164:165], s[12:13], 0, v[172:173]
	v_lshlrev_b64 v[172:173], 12, v[174:175]
	v_lshlrev_b64 v[174:175], 12, v[176:177]
	v_lshlrev_b64 v[176:177], 12, v[178:179]
	v_lshl_add_u64 v[172:173], s[12:13], 0, v[172:173]
	v_lshl_add_u64 v[174:175], s[12:13], 0, v[174:175]
	v_lshl_add_u64 v[176:177], s[12:13], 0, v[176:177]
	v_lshl_add_u64 v[164:165], v[164:165], 0, v[180:181]
	v_lshl_add_u64 v[172:173], v[172:173], 0, v[180:181]
	v_lshl_add_u64 v[174:175], v[174:175], 0, v[180:181]
	v_lshl_add_u64 v[176:177], v[176:177], 0, v[180:181]
	s_waitcnt vmcnt(0)
	v_pk_mul_f32 v[124:125], v[124:125], v[144:145]
	v_pk_mul_f32 v[122:123], v[122:123], v[142:143]
	v_pk_mul_f32 v[180:181], v[72:73], v[136:137]
	v_cvt_pk_bf16_f32 v72, v122, v123
	v_cvt_pk_bf16_f32 v73, v124, v125
	v_pk_mul_f32 v[128:129], v[128:129], v[140:141]
	v_pk_mul_f32 v[126:127], v[126:127], v[138:139]
	v_pk_mul_f32 v[120:121], v[120:121], v[136:137]
	v_pk_mul_f32 v[118:119], v[118:119], v[134:135]
	v_pk_mul_f32 v[178:179], v[74:75], v[138:139]
	v_cvt_pk_bf16_f32 v74, v126, v127
	v_cvt_pk_bf16_f32 v75, v128, v129
	global_store_dwordx4 v[164:165], v[72:75], off
	v_pk_mul_f32 v[116:117], v[116:117], v[132:133]
	v_pk_mul_f32 v[114:115], v[114:115], v[130:131]
	v_cvt_pk_bf16_f32 v72, v118, v119
	v_cvt_pk_bf16_f32 v73, v120, v121
	v_pk_mul_f32 v[112:113], v[112:113], v[144:145]
	v_pk_mul_f32 v[110:111], v[110:111], v[142:143]
	v_cvt_pk_bf16_f32 v74, v114, v115
	v_cvt_pk_bf16_f32 v75, v116, v117
	global_store_dwordx4 v[164:165], v[72:75], off offset:64
	v_pk_mul_f32 v[108:109], v[108:109], v[140:141]
	v_pk_mul_f32 v[106:107], v[106:107], v[138:139]
	v_cvt_pk_bf16_f32 v72, v110, v111
	v_cvt_pk_bf16_f32 v73, v112, v113
	v_pk_mul_f32 v[104:105], v[104:105], v[136:137]
	v_pk_mul_f32 v[102:103], v[102:103], v[134:135]
	v_cvt_pk_bf16_f32 v74, v106, v107
	v_cvt_pk_bf16_f32 v75, v108, v109
	global_store_dwordx4 v[172:173], v[72:75], off
	v_pk_mul_f32 v[100:101], v[100:101], v[132:133]
	v_pk_mul_f32 v[98:99], v[98:99], v[130:131]
	v_cvt_pk_bf16_f32 v72, v102, v103
	v_cvt_pk_bf16_f32 v73, v104, v105
	v_pk_mul_f32 v[96:97], v[96:97], v[144:145]
	v_pk_mul_f32 v[94:95], v[94:95], v[142:143]
	v_cvt_pk_bf16_f32 v74, v98, v99
	v_cvt_pk_bf16_f32 v75, v100, v101
	global_store_dwordx4 v[172:173], v[72:75], off offset:64
	v_pk_mul_f32 v[92:93], v[92:93], v[140:141]
	v_pk_mul_f32 v[90:91], v[90:91], v[138:139]
	v_cvt_pk_bf16_f32 v72, v94, v95
	v_cvt_pk_bf16_f32 v73, v96, v97
	v_pk_mul_f32 v[88:89], v[88:89], v[136:137]
	v_pk_mul_f32 v[86:87], v[86:87], v[134:135]
	v_cvt_pk_bf16_f32 v74, v90, v91
	v_cvt_pk_bf16_f32 v75, v92, v93
	global_store_dwordx4 v[174:175], v[72:75], off
	v_pk_mul_f32 v[84:85], v[84:85], v[132:133]
	v_pk_mul_f32 v[82:83], v[82:83], v[130:131]
	v_cvt_pk_bf16_f32 v72, v86, v87
	v_cvt_pk_bf16_f32 v73, v88, v89
	v_pk_mul_f32 v[80:81], v[80:81], v[144:145]
	v_pk_mul_f32 v[78:79], v[78:79], v[142:143]
	v_cvt_pk_bf16_f32 v74, v82, v83
	v_cvt_pk_bf16_f32 v75, v84, v85
	global_store_dwordx4 v[174:175], v[72:75], off offset:64
	v_pk_mul_f32 v[76:77], v[76:77], v[140:141]
	v_pk_mul_f32 v[70:71], v[70:71], v[134:135]
	v_cvt_pk_bf16_f32 v72, v78, v79
	v_cvt_pk_bf16_f32 v73, v80, v81
	v_cvt_pk_bf16_f32 v74, v178, v179
	v_cvt_pk_bf16_f32 v75, v76, v77
	global_store_dwordx4 v[176:177], v[72:75], off
	v_pk_mul_f32 v[62:63], v[62:63], v[142:143]
	v_pk_mul_f32 v[64:65], v[64:65], v[144:145]
	v_pk_mul_f32 v[72:73], v[68:69], v[132:133]
	v_pk_mul_f32 v[68:69], v[66:67], v[130:131]
	v_cvt_pk_bf16_f32 v66, v70, v71
	v_cvt_pk_bf16_f32 v67, v180, v181
	v_pk_mul_f32 v[56:57], v[56:57], v[136:137]
	v_cvt_pk_bf16_f32 v68, v68, v69
	v_cvt_pk_bf16_f32 v69, v72, v73
	global_store_dwordx4 v[176:177], v[66:69], off offset:64
	v_pk_mul_f32 v[54:55], v[54:55], v[134:135]
	v_pk_mul_f32 v[46:47], v[46:47], v[142:143]
	v_pk_mul_f32 v[68:69], v[60:61], v[140:141]
	v_pk_mul_f32 v[60:61], v[58:59], v[138:139]
	v_cvt_pk_bf16_f32 v58, v62, v63
	v_add_co_u32_e32 v62, vcc, s59, v164
	v_cvt_pk_bf16_f32 v59, v64, v65
	v_cvt_pk_bf16_f32 v60, v60, v61
	v_cvt_pk_bf16_f32 v61, v68, v69
	v_lshl_add_u64 v[66:67], v[164:165], 0, s[24:25]
	s_nop 0
	v_addc_co_u32_e32 v63, vcc, 0, v165, vcc
	global_store_dwordx4 v[62:63], v[58:61], off
	v_pk_mul_f32 v[48:49], v[48:49], v[144:145]
	v_pk_mul_f32 v[40:41], v[40:41], v[136:137]
	v_pk_mul_f32 v[58:59], v[52:53], v[132:133]
	v_pk_mul_f32 v[52:53], v[50:51], v[130:131]
	v_cvt_pk_bf16_f32 v50, v54, v55
	v_cvt_pk_bf16_f32 v51, v56, v57
	v_pk_mul_f32 v[38:39], v[38:39], v[134:135]
	v_cvt_pk_bf16_f32 v52, v52, v53
	v_cvt_pk_bf16_f32 v53, v58, v59
	global_store_dwordx4 v[66:67], v[50:53], off offset:64
	v_pk_mul_f32 v[30:31], v[30:31], v[142:143]
	v_pk_mul_f32 v[32:33], v[32:33], v[144:145]
	v_pk_mul_f32 v[52:53], v[44:45], v[140:141]
	v_pk_mul_f32 v[44:45], v[42:43], v[138:139]
	v_cvt_pk_bf16_f32 v42, v46, v47
	v_add_co_u32_e32 v46, vcc, s60, v164
	v_cvt_pk_bf16_f32 v43, v48, v49
	v_cvt_pk_bf16_f32 v44, v44, v45
	v_cvt_pk_bf16_f32 v45, v52, v53
	v_lshl_add_u64 v[50:51], v[164:165], 0, s[26:27]
	s_nop 0
	v_addc_co_u32_e32 v47, vcc, 0, v165, vcc
	global_store_dwordx4 v[46:47], v[42:45], off
	v_pk_mul_f32 v[24:25], v[24:25], v[136:137]
	v_pk_mul_f32 v[22:23], v[22:23], v[134:135]
	v_pk_mul_f32 v[42:43], v[36:37], v[132:133]
	v_pk_mul_f32 v[36:37], v[34:35], v[130:131]
	v_cvt_pk_bf16_f32 v34, v38, v39
	v_cvt_pk_bf16_f32 v35, v40, v41
	v_pk_mul_f32 v[14:15], v[14:15], v[142:143]
	v_cvt_pk_bf16_f32 v36, v36, v37
	v_cvt_pk_bf16_f32 v37, v42, v43
	global_store_dwordx4 v[50:51], v[34:37], off offset:64
	v_pk_mul_f32 v[16:17], v[16:17], v[144:145]
	v_pk_mul_f32 v[8:9], v[8:9], v[136:137]
	v_pk_mul_f32 v[36:37], v[28:29], v[140:141]
	v_pk_mul_f32 v[28:29], v[26:27], v[138:139]
	v_cvt_pk_bf16_f32 v26, v30, v31
	v_add_co_u32_e32 v30, vcc, s61, v164
	v_cvt_pk_bf16_f32 v27, v32, v33
	v_cvt_pk_bf16_f32 v28, v28, v29
	v_cvt_pk_bf16_f32 v29, v36, v37
	v_lshl_add_u64 v[34:35], v[164:165], 0, s[28:29]
	s_nop 0
	v_addc_co_u32_e32 v31, vcc, 0, v165, vcc
	global_store_dwordx4 v[30:31], v[26:29], off
	v_pk_mul_f32 v[6:7], v[6:7], v[134:135]
	s_nop 0
	v_pk_mul_f32 v[26:27], v[20:21], v[132:133]
	v_pk_mul_f32 v[20:21], v[18:19], v[130:131]
	v_cvt_pk_bf16_f32 v18, v22, v23
	v_cvt_pk_bf16_f32 v19, v24, v25
	s_nop 0
	v_cvt_pk_bf16_f32 v20, v20, v21
	v_cvt_pk_bf16_f32 v21, v26, v27
	global_store_dwordx4 v[34:35], v[18:21], off offset:64
	s_nop 1
	v_pk_mul_f32 v[20:21], v[12:13], v[140:141]
	v_pk_mul_f32 v[12:13], v[10:11], v[138:139]
	v_cvt_pk_bf16_f32 v10, v14, v15
	v_add_co_u32_e32 v14, vcc, s62, v164
	v_cvt_pk_bf16_f32 v11, v16, v17
	v_lshl_add_u64 v[18:19], v[164:165], 0, s[30:31]
	s_nop 0
	v_addc_co_u32_e32 v15, vcc, 0, v165, vcc
	v_cvt_pk_bf16_f32 v12, v12, v13
	v_cvt_pk_bf16_f32 v13, v20, v21
	global_store_dwordx4 v[14:15], v[10:13], off
	s_and_b64 vcc, exec, s[0:1]
	s_mov_b64 s[0:1], -1
	v_pk_mul_f32 v[10:11], v[4:5], v[132:133]
	v_pk_mul_f32 v[4:5], v[2:3], v[130:131]
	v_cvt_pk_bf16_f32 v2, v6, v7
	v_cvt_pk_bf16_f32 v3, v8, v9
	s_nop 0
	v_cvt_pk_bf16_f32 v4, v4, v5
	v_cvt_pk_bf16_f32 v5, v10, v11
	global_store_dwordx4 v[18:19], v[2:5], off offset:64
	s_mov_b32 s100, 1
	s_cbranch_vccnz .LBB0_1063
	s_andn2_b64 vcc, exec, s[10:11]
	s_cbranch_vccnz .LBB0_1062
	s_barrier
	s_branch .LBB0_1062

.LBB0_1294:
	s_mov_b32 s101, 0
	s_cmp_lt_i32 s60, 10
	s_cselect_b64 s[4:5], -1, 0
	s_and_b64 s[0:1], s[4:5], s[0:1]
	s_andn2_b64 vcc, exec, s[0:1]
	s_cbranch_vccnz .LBB0_1371
	s_cmpk_gt_u32 s63, 0x7f
	s_waitcnt vmcnt(0) lgkmcnt(0)
	s_barrier
	s_cbranch_scc1 .LBB0_1299
	s_mul_i32 s0, s97, 0x108
	s_add_i32 s2, s0, 0
	s_and_b32 s0, s63, 64
	v_readlane_b32 s8, v252, 2
	s_add_i32 s2, s2, 0x24000
	s_lshl_b32 s0, s0, 2
	v_readlane_b32 s10, v252, 4
	v_readlane_b32 s11, v252, 5
	s_add_u32 s0, s10, s0
	v_lshlrev_b32_e32 v2, 2, v206
	s_addc_u32 s1, s11, 0
	v_mov_b32_e32 v3, 0
	v_lshl_add_u64 v[4:5], s[0:1], 0, v[2:3]
	v_add_co_u32_e32 v4, vcc, 0x10000, v4
	v_mbcnt_lo_u32_b32 v3, -1, 0
	s_nop 0
	v_addc_co_u32_e32 v5, vcc, 0, v5, vcc
	global_load_dword v1, v[4:5], off sc1
	v_mbcnt_hi_u32_b32 v3, -1, v3
	v_and_b32_e32 v4, 64, v3
	v_add_u32_e32 v5, -1, v3
	v_cmp_lt_i32_e32 vcc, v5, v4
	v_add_u32_e32 v6, -2, v3
	v_add_u32_e32 v7, -4, v3
	v_cndmask_b32_e32 v5, v5, v3, vcc
	v_lshlrev_b32_e32 v5, 2, v5
	v_cmp_lt_i32_e32 vcc, v6, v4
	v_add_u32_e32 v8, -8, v3
	v_add_u32_e32 v9, -16, v3
	v_cndmask_b32_e32 v6, v6, v3, vcc
	v_cmp_ne_u32_e32 vcc, 0, v206
	v_lshlrev_b32_e32 v6, 2, v6
	v_cmp_lt_u32_e64 s[0:1], 31, v206
	v_readlane_b32 s9, v252, 3
	s_waitcnt vmcnt(0)
	v_add_u32_e32 v1, 0xff, v1
	v_and_b32_e32 v1, 0xffffff00, v1
	ds_bpermute_b32 v5, v5, v1
	s_waitcnt lgkmcnt(0)
	v_cndmask_b32_e32 v5, 0, v5, vcc
	v_add_u32_e32 v5, v5, v1
	ds_bpermute_b32 v6, v6, v5
	v_cmp_lt_i32_e32 vcc, v7, v4
	s_nop 1
	v_cndmask_b32_e32 v7, v7, v3, vcc
	v_cmp_lt_u32_e32 vcc, 1, v206
	v_lshlrev_b32_e32 v7, 2, v7
	s_waitcnt lgkmcnt(0)
	v_cndmask_b32_e32 v6, 0, v6, vcc
	v_add_u32_e32 v5, v6, v5
	ds_bpermute_b32 v6, v7, v5
	v_cmp_lt_i32_e32 vcc, v8, v4
	s_nop 1
	v_cndmask_b32_e32 v7, v8, v3, vcc
	v_cmp_lt_u32_e32 vcc, 3, v206
	v_lshlrev_b32_e32 v7, 2, v7
	s_waitcnt lgkmcnt(0)
	v_cndmask_b32_e32 v6, 0, v6, vcc
	v_add_u32_e32 v5, v6, v5
	ds_bpermute_b32 v6, v7, v5
	v_cmp_lt_i32_e32 vcc, v9, v4
	s_nop 1
	v_cndmask_b32_e32 v7, v9, v3, vcc
	v_cmp_lt_u32_e32 vcc, 7, v206
	v_lshlrev_b32_e32 v7, 2, v7
	s_waitcnt lgkmcnt(0)
	v_cndmask_b32_e32 v6, 0, v6, vcc
	v_add_u32_e32 v5, v6, v5
	ds_bpermute_b32 v6, v7, v5
	v_subrev_u32_e32 v7, 32, v3
	v_cmp_lt_i32_e32 vcc, v7, v4
	s_nop 1
	v_cndmask_b32_e32 v3, v7, v3, vcc
	v_cmp_lt_u32_e32 vcc, 15, v206
	v_lshlrev_b32_e32 v3, 2, v3
	s_waitcnt lgkmcnt(0)
	v_cndmask_b32_e32 v4, 0, v6, vcc
	v_add_u32_e32 v4, v4, v5
	ds_bpermute_b32 v3, v3, v4
	v_add_u32_e32 v5, s2, v2
	v_cmp_eq_u32_e32 vcc, 63, v206
	s_waitcnt lgkmcnt(0)
	v_cndmask_b32_e64 v2, 0, v3, s[0:1]
	v_add_u32_e32 v2, v2, v4
	v_sub_u32_e32 v1, v2, v1
	ds_write_b32 v5, v1
	s_and_saveexec_b64 s[0:1], vcc
	v_add_u32_e32 v3, 0x4000, v2
	v_mov_b32_e32 v1, s2
	ds_write_b64 v1, v[2:3] offset:256
	s_or_b64 exec, exec, s[0:1]

.LBB0_1362:
	s_and_b64 vcc, exec, s[0:1]
	s_cmp_eq_u32 s101, 0
	s_cbranch_scc1 .Lgk_first_p9
	v_mov_b32_e32 v175, v169
	v_mov_b32_e32 v173, v169
	s_mov_b32 s21, 0
	s_mov_b64 s[30:31], 0x100
	s_mov_b64 s[34:35], s[14:15]
	ds_read_b128 v[26:29], v191
	ds_read_b128 v[30:33], v191 offset:1024
	ds_read_b128 v[18:21], v191 offset:2048
	ds_read_b128 v[22:25], v191 offset:3072
	ds_read_b128 v[10:13], v192
	ds_read_b128 v[14:17], v192 offset:1024
	ds_read_b128 v[2:5], v192 offset:2048
	ds_read_b128 v[6:9], v192 offset:3072
	s_cmp_eq_u32 s55, s21
	s_cselect_b64 vcc, -1, 0
	s_add_i32 s21, s21, 2
	s_and_b64 s[36:37], vcc, exec
	s_cselect_b32 s36, 0, s30
	s_cselect_b32 s23, 0, s31
	s_add_u32 s36, s8, s36
	s_addc_u32 s37, s9, s23
	s_add_u32 s23, s28, s30
	s_addc_u32 s70, s29, s31
	s_and_b64 s[38:39], vcc, exec
	v_cndmask_b32_e32 v168, v197, v198, vcc
	v_cndmask_b32_e32 v202, v172, v200, vcc
	v_cndmask_b32_e32 v184, v170, v199, vcc
	s_cselect_b32 s39, s25, s70
	s_cselect_b32 s38, s24, s23
	s_mov_b32 m0, s56
	v_lshl_add_u64 v[186:187], s[34:35], 0, v[172:173]
	ds_read_b128 v[176:179], v193
	ds_read_b128 v[180:183], v193 offset:1024
	ds_read_b128 v[208:211], v193 offset:2048
	ds_read_b128 v[212:215], v193 offset:3072
	ds_read_b128 v[216:219], v193 offset:4096
	ds_read_b128 v[220:223], v193 offset:5120
	ds_read_b128 v[224:227], v193 offset:6144
	ds_read_b128 v[228:231], v193 offset:7168
	global_load_lds_dwordx4 v[186:187], off
	v_lshl_add_u64 v[186:187], s[34:35], 0, v[174:175]
	s_mov_b32 m0, s57
	s_nop 0
	global_load_lds_dwordx4 v[186:187], off
	s_waitcnt vmcnt(16)
	s_waitcnt lgkmcnt(0)
	s_barrier
	s_setprio 1
	s_waitcnt lgkmcnt(0)
	v_mfma_scale_f32_16x16x128_f8f6f4 v[154:157], v[26:33], v[176:183], 0, v188, v189 op_sel_hi:[0,0,0]
	v_mfma_scale_f32_16x16x128_f8f6f4 v[150:153], v[18:25], v[176:183], 0, v188, v189 op_sel_hi:[0,0,0]
	v_mfma_scale_f32_16x16x128_f8f6f4 v[142:145], v[26:33], v[208:215], 0, v188, v189 op_sel_hi:[0,0,0]
	v_mfma_scale_f32_16x16x128_f8f6f4 v[134:137], v[18:25], v[208:215], 0, v188, v189 op_sel_hi:[0,0,0]
	v_mfma_scale_f32_16x16x128_f8f6f4 v[126:129], v[26:33], v[216:223], 0, v188, v189 op_sel_hi:[0,0,0]
	v_mfma_scale_f32_16x16x128_f8f6f4 v[118:121], v[18:25], v[216:223], 0, v188, v189 op_sel_hi:[0,0,0]
	v_mfma_scale_f32_16x16x128_f8f6f4 v[110:113], v[26:33], v[224:231], 0, v188, v189 op_sel_hi:[0,0,0]
	v_mfma_scale_f32_16x16x128_f8f6f4 v[102:105], v[18:25], v[224:231], 0, v188, v189 op_sel_hi:[0,0,0]
	s_setprio 0
	s_setprio 1
	v_mfma_scale_f32_16x16x128_f8f6f4 v[158:161], v[10:17], v[176:183], 0, v188, v189 op_sel_hi:[0,0,0]
	v_mfma_scale_f32_16x16x128_f8f6f4 v[146:149], v[2:9], v[176:183], 0, v188, v189 op_sel_hi:[0,0,0]
	v_mfma_scale_f32_16x16x128_f8f6f4 v[138:141], v[10:17], v[208:215], 0, v188, v189 op_sel_hi:[0,0,0]
	v_mfma_scale_f32_16x16x128_f8f6f4 v[130:133], v[2:9], v[208:215], 0, v188, v189 op_sel_hi:[0,0,0]
	v_mfma_scale_f32_16x16x128_f8f6f4 v[122:125], v[10:17], v[216:223], 0, v188, v189 op_sel_hi:[0,0,0]
	v_mfma_scale_f32_16x16x128_f8f6f4 v[114:117], v[2:9], v[216:223], 0, v188, v189 op_sel_hi:[0,0,0]
	v_mfma_scale_f32_16x16x128_f8f6f4 v[106:109], v[10:17], v[224:231], 0, v188, v189 op_sel_hi:[0,0,0]
	v_mfma_scale_f32_16x16x128_f8f6f4 v[98:101], v[2:9], v[224:231], 0, v188, v189 op_sel_hi:[0,0,0]
	s_setprio 0
	s_barrier
	s_mov_b32 m0, s58
	v_lshl_add_u64 v[176:177], s[38:39], 0, v[166:167]
	v_lshl_add_u64 v[178:179], s[38:39], 0, v[164:165]
	s_add_u32 s38, s38, s6
	ds_read_b128 v[208:211], v193 offset:16384
	ds_read_b128 v[212:215], v193 offset:17408
	ds_read_b128 v[216:219], v193 offset:18432
	ds_read_b128 v[220:223], v193 offset:19456
	ds_read_b128 v[224:227], v193 offset:20480
	ds_read_b128 v[228:231], v193 offset:21504
	ds_read_b128 v[232:235], v193 offset:22528
	ds_read_b128 v[236:239], v193 offset:23552
	global_load_lds_dwordx4 v[176:177], off
	s_mov_b32 m0, s59
	s_addc_u32 s39, s39, s7
	global_load_lds_dwordx4 v[178:179], off
	v_lshl_add_u64 v[180:181], s[38:39], 0, v[166:167]
	s_mov_b32 m0, s60
	v_lshl_add_u64 v[182:183], s[38:39], 0, v[164:165]
	global_load_lds_dwordx4 v[180:181], off
	s_mov_b32 m0, s61
	v_mov_b32_e32 v185, v169
	global_load_lds_dwordx4 v[182:183], off
	s_mov_b32 m0, s27
	v_lshl_add_u64 v[186:187], s[36:37], 0, v[168:169]
	global_load_lds_dwordx4 v168, s[36:37]
	s_mov_b32 m0, s45
	s_nop 0
	global_load_lds_dwordx4 v184, s[36:37]
	s_waitcnt vmcnt(16)
	s_waitcnt lgkmcnt(0)
	v_lshl_add_u64 v[184:185], s[36:37], 0, v[184:185]
	s_barrier
	s_setprio 1
	s_waitcnt lgkmcnt(0)
	v_mfma_scale_f32_16x16x128_f8f6f4 v[94:97], v[26:33], v[208:215], 0, v188, v189 op_sel_hi:[0,0,0]
	v_mfma_scale_f32_16x16x128_f8f6f4 v[86:89], v[18:25], v[208:215], 0, v188, v189 op_sel_hi:[0,0,0]
	v_mfma_scale_f32_16x16x128_f8f6f4 v[78:81], v[26:33], v[216:223], 0, v188, v189 op_sel_hi:[0,0,0]
	v_mfma_scale_f32_16x16x128_f8f6f4 v[70:73], v[18:25], v[216:223], 0, v188, v189 op_sel_hi:[0,0,0]
	v_mfma_scale_f32_16x16x128_f8f6f4 v[62:65], v[26:33], v[224:231], 0, v188, v189 op_sel_hi:[0,0,0]
	v_mfma_scale_f32_16x16x128_f8f6f4 v[54:57], v[18:25], v[224:231], 0, v188, v189 op_sel_hi:[0,0,0]
	v_mfma_scale_f32_16x16x128_f8f6f4 v[46:49], v[26:33], v[232:239], 0, v188, v189 op_sel_hi:[0,0,0]
	v_mfma_scale_f32_16x16x128_f8f6f4 v[38:41], v[18:25], v[232:239], 0, v188, v189 op_sel_hi:[0,0,0]
	s_setprio 0
	s_setprio 1
	v_mfma_scale_f32_16x16x128_f8f6f4 v[90:93], v[10:17], v[208:215], 0, v188, v189 op_sel_hi:[0,0,0]
	v_mfma_scale_f32_16x16x128_f8f6f4 v[82:85], v[2:9], v[208:215], 0, v188, v189 op_sel_hi:[0,0,0]
	v_mfma_scale_f32_16x16x128_f8f6f4 v[74:77], v[10:17], v[216:223], 0, v188, v189 op_sel_hi:[0,0,0]
	v_mfma_scale_f32_16x16x128_f8f6f4 v[66:69], v[2:9], v[216:223], 0, v188, v189 op_sel_hi:[0,0,0]
	v_mfma_scale_f32_16x16x128_f8f6f4 v[58:61], v[10:17], v[224:231], 0, v188, v189 op_sel_hi:[0,0,0]
	v_mfma_scale_f32_16x16x128_f8f6f4 v[50:53], v[2:9], v[224:231], 0, v188, v189 op_sel_hi:[0,0,0]
	v_mfma_scale_f32_16x16x128_f8f6f4 v[42:45], v[10:17], v[232:239], 0, v188, v189 op_sel_hi:[0,0,0]
	v_mfma_scale_f32_16x16x128_f8f6f4 v[34:37], v[2:9], v[232:239], 0, v188, v189 op_sel_hi:[0,0,0]
	s_setprio 0
	s_barrier
	ds_read_b128 v[26:29], v194
	ds_read_b128 v[30:33], v194 offset:1024
	ds_read_b128 v[18:21], v194 offset:2048
	ds_read_b128 v[22:25], v194 offset:3072
	ds_read_b128 v[10:13], v195
	ds_read_b128 v[14:17], v195 offset:1024
	ds_read_b128 v[2:5], v195 offset:2048
	ds_read_b128 v[6:9], v195 offset:3072
	s_mov_b32 m0, s46
	ds_read_b128 v[208:211], v193 offset:32768
	ds_read_b128 v[212:215], v193 offset:33792
	ds_read_b128 v[216:219], v193 offset:34816
	ds_read_b128 v[220:223], v193 offset:35840
	ds_read_b128 v[224:227], v193 offset:36864
	ds_read_b128 v[228:231], v193 offset:37888
	ds_read_b128 v[232:235], v193 offset:38912
	ds_read_b128 v[236:239], v193 offset:39936
	v_cndmask_b32_e32 v168, v174, v201, vcc
	global_load_lds_dwordx4 v202, s[36:37]
	s_mov_b32 m0, s47
	s_nop 0
	global_load_lds_dwordx4 v168, s[36:37]
	s_waitcnt vmcnt(8)
	s_waitcnt lgkmcnt(0)
	s_barrier
	s_setprio 1
	s_waitcnt lgkmcnt(0)
	v_mfma_scale_f32_16x16x128_f8f6f4 v[154:157], v[26:33], v[208:215], v[154:157], v188, v189 op_sel_hi:[0,0,0]
	v_mfma_scale_f32_16x16x128_f8f6f4 v[150:153], v[18:25], v[208:215], v[150:153], v188, v189 op_sel_hi:[0,0,0]
	v_mfma_scale_f32_16x16x128_f8f6f4 v[142:145], v[26:33], v[216:223], v[142:145], v188, v189 op_sel_hi:[0,0,0]
	v_mfma_scale_f32_16x16x128_f8f6f4 v[134:137], v[18:25], v[216:223], v[134:137], v188, v189 op_sel_hi:[0,0,0]
	v_mfma_scale_f32_16x16x128_f8f6f4 v[126:129], v[26:33], v[224:231], v[126:129], v188, v189 op_sel_hi:[0,0,0]
	v_mfma_scale_f32_16x16x128_f8f6f4 v[118:121], v[18:25], v[224:231], v[118:121], v188, v189 op_sel_hi:[0,0,0]
	v_mfma_scale_f32_16x16x128_f8f6f4 v[110:113], v[26:33], v[232:239], v[110:113], v188, v189 op_sel_hi:[0,0,0]
	v_mfma_scale_f32_16x16x128_f8f6f4 v[102:105], v[18:25], v[232:239], v[102:105], v188, v189 op_sel_hi:[0,0,0]
	s_setprio 0
	s_setprio 1
	v_mfma_scale_f32_16x16x128_f8f6f4 v[158:161], v[10:17], v[208:215], v[158:161], v188, v189 op_sel_hi:[0,0,0]
	v_mfma_scale_f32_16x16x128_f8f6f4 v[146:149], v[2:9], v[208:215], v[146:149], v188, v189 op_sel_hi:[0,0,0]
	v_mfma_scale_f32_16x16x128_f8f6f4 v[138:141], v[10:17], v[216:223], v[138:141], v188, v189 op_sel_hi:[0,0,0]
	v_mfma_scale_f32_16x16x128_f8f6f4 v[130:133], v[2:9], v[216:223], v[130:133], v188, v189 op_sel_hi:[0,0,0]
	v_mfma_scale_f32_16x16x128_f8f6f4 v[122:125], v[10:17], v[224:231], v[122:125], v188, v189 op_sel_hi:[0,0,0]
	v_mfma_scale_f32_16x16x128_f8f6f4 v[114:117], v[2:9], v[224:231], v[114:117], v188, v189 op_sel_hi:[0,0,0]
	v_mfma_scale_f32_16x16x128_f8f6f4 v[106:109], v[10:17], v[232:239], v[106:109], v188, v189 op_sel_hi:[0,0,0]
	v_mfma_scale_f32_16x16x128_f8f6f4 v[98:101], v[2:9], v[232:239], v[98:101], v188, v189 op_sel_hi:[0,0,0]
	s_setprio 0
	s_barrier
	s_mov_b32 m0, s63
	v_lshl_add_u64 v[176:177], v[176:177], 0, s[16:17]
	ds_read_b128 v[208:211], v193 offset:49152
	ds_read_b128 v[212:215], v193 offset:50176
	ds_read_b128 v[216:219], v193 offset:51200
	ds_read_b128 v[220:223], v193 offset:52224
	ds_read_b128 v[224:227], v193 offset:53248
	ds_read_b128 v[228:231], v193 offset:54272
	ds_read_b128 v[232:235], v193 offset:55296
	ds_read_b128 v[236:239], v193 offset:56320
	global_load_lds_dwordx4 v[176:177], off
	v_lshl_add_u64 v[176:177], v[178:179], 0, s[16:17]
	s_mov_b32 m0, s64
	s_nop 0
	global_load_lds_dwordx4 v[176:177], off
	v_lshl_add_u64 v[176:177], v[180:181], 0, s[16:17]
	s_mov_b32 m0, s65
	s_nop 0
	global_load_lds_dwordx4 v[176:177], off
	v_lshl_add_u64 v[176:177], v[182:183], 0, s[16:17]
	s_mov_b32 m0, s66
	s_nop 0
	global_load_lds_dwordx4 v[176:177], off
	v_lshl_add_u64 v[176:177], v[186:187], 0, s[16:17]
	s_mov_b32 m0, s53
	s_nop 0
	global_load_lds_dwordx4 v[176:177], off
	v_lshl_add_u64 v[176:177], v[184:185], 0, s[16:17]
	s_mov_b32 m0, s54
	s_nop 0
	global_load_lds_dwordx4 v[176:177], off
	s_waitcnt vmcnt(8)
	s_waitcnt lgkmcnt(0)
	s_barrier
	s_setprio 1
	s_waitcnt lgkmcnt(0)
	v_mfma_scale_f32_16x16x128_f8f6f4 v[94:97], v[26:33], v[208:215], v[94:97], v188, v189 op_sel_hi:[0,0,0]
	v_mfma_scale_f32_16x16x128_f8f6f4 v[86:89], v[18:25], v[208:215], v[86:89], v188, v189 op_sel_hi:[0,0,0]
	v_mfma_scale_f32_16x16x128_f8f6f4 v[78:81], v[26:33], v[216:223], v[78:81], v188, v189 op_sel_hi:[0,0,0]
	v_mfma_scale_f32_16x16x128_f8f6f4 v[70:73], v[18:25], v[216:223], v[70:73], v188, v189 op_sel_hi:[0,0,0]
	v_mfma_scale_f32_16x16x128_f8f6f4 v[62:65], v[26:33], v[224:231], v[62:65], v188, v189 op_sel_hi:[0,0,0]
	v_mfma_scale_f32_16x16x128_f8f6f4 v[54:57], v[18:25], v[224:231], v[54:57], v188, v189 op_sel_hi:[0,0,0]
	v_mfma_scale_f32_16x16x128_f8f6f4 v[46:49], v[26:33], v[232:239], v[46:49], v188, v189 op_sel_hi:[0,0,0]
	v_mfma_scale_f32_16x16x128_f8f6f4 v[38:41], v[18:25], v[232:239], v[38:41], v188, v189 op_sel_hi:[0,0,0]
	s_setprio 0
	s_setprio 1
	v_mfma_scale_f32_16x16x128_f8f6f4 v[90:93], v[10:17], v[208:215], v[90:93], v188, v189 op_sel_hi:[0,0,0]
	v_mfma_scale_f32_16x16x128_f8f6f4 v[82:85], v[2:9], v[208:215], v[82:85], v188, v189 op_sel_hi:[0,0,0]
	v_mfma_scale_f32_16x16x128_f8f6f4 v[74:77], v[10:17], v[216:223], v[74:77], v188, v189 op_sel_hi:[0,0,0]
	v_mfma_scale_f32_16x16x128_f8f6f4 v[66:69], v[2:9], v[216:223], v[66:69], v188, v189 op_sel_hi:[0,0,0]
	v_mfma_scale_f32_16x16x128_f8f6f4 v[58:61], v[10:17], v[224:231], v[58:61], v188, v189 op_sel_hi:[0,0,0]
	v_mfma_scale_f32_16x16x128_f8f6f4 v[50:53], v[2:9], v[224:231], v[50:53], v188, v189 op_sel_hi:[0,0,0]
	v_mfma_scale_f32_16x16x128_f8f6f4 v[42:45], v[10:17], v[232:239], v[42:45], v188, v189 op_sel_hi:[0,0,0]
	v_mfma_scale_f32_16x16x128_f8f6f4 v[34:37], v[2:9], v[232:239], v[34:37], v188, v189 op_sel_hi:[0,0,0]
	s_setprio 0
	s_barrier
	s_add_u32 s30, s30, 0x100
	s_addc_u32 s31, s31, 0
	s_add_u32 s34, s34, 0x100
	s_addc_u32 s35, s35, 0
	s_cmp_ge_i32 s21, s52
	s_cbranch_scc1 .LBB0_1365
	s_branch .LBB0_1364

.LBB0_1367:
	v_lshl_add_u32 v6, s69, 8, v171
	v_mul_f32_e32 v2, 0xbcb8aa3b, v154
	v_exp_f32_e32 v2, v2
	v_mul_f32_e32 v8, 0xbcb8aa3b, v155
	v_exp_f32_e32 v8, v8
	v_mul_f32_e32 v3, v154, v158
	v_add_f32_e32 v2, 1.0, v2
	v_rcp_f32_e32 v2, v2
	v_add_f32_e32 v8, 1.0, v8
	v_rcp_f32_e32 v8, v8
	v_mul_f32_e32 v3, 0x3a800000, v3
	v_mul_f32_e32 v2, v3, v2
	v_mul_f32_e32 v3, v155, v159
	v_mul_f32_e32 v3, 0x3a800000, v3
	v_mul_f32_e32 v3, v3, v8
	v_mul_f32_e32 v8, 0xbcb8aa3b, v156
	v_exp_f32_e32 v8, v8
	v_mul_f32_e32 v10, 0xbcb8aa3b, v157
	v_exp_f32_e32 v10, v10
	v_mul_f32_e32 v9, v156, v160
	v_add_f32_e32 v8, 1.0, v8
	v_rcp_f32_e32 v8, v8
	v_add_f32_e32 v10, 1.0, v10
	v_rcp_f32_e32 v10, v10
	v_mul_f32_e32 v9, 0x3a800000, v9
	v_mul_f32_e32 v8, v9, v8
	v_mul_f32_e32 v9, v157, v161
	v_mul_f32_e32 v9, 0x3a800000, v9
	v_mul_f32_e32 v9, v9, v10
	v_mul_f32_e32 v10, 0xbcb8aa3b, v150
	v_exp_f32_e32 v10, v10
	v_mul_f32_e32 v12, 0xbcb8aa3b, v151
	v_exp_f32_e32 v12, v12
	v_mul_f32_e32 v11, v150, v146
	v_add_f32_e32 v10, 1.0, v10
	v_rcp_f32_e32 v10, v10
	v_add_f32_e32 v12, 1.0, v12
	v_rcp_f32_e32 v12, v12
	v_mul_f32_e32 v11, 0x3a800000, v11
	v_mul_f32_e32 v10, v11, v10
	v_mul_f32_e32 v11, v151, v147
	v_mul_f32_e32 v11, 0x3a800000, v11
	v_mul_f32_e32 v11, v11, v12
	v_mul_f32_e32 v12, 0xbcb8aa3b, v152
	v_exp_f32_e32 v12, v12
	v_mul_f32_e32 v14, 0xbcb8aa3b, v153
	v_exp_f32_e32 v14, v14
	v_mul_f32_e32 v13, v152, v148
	v_add_f32_e32 v12, 1.0, v12
	v_rcp_f32_e32 v12, v12
	v_add_f32_e32 v14, 1.0, v14
	v_rcp_f32_e32 v14, v14
	v_mul_f32_e32 v13, 0x3a800000, v13
	v_mul_f32_e32 v12, v13, v12
	v_mul_f32_e32 v13, v153, v149
	v_mul_f32_e32 v13, 0x3a800000, v13
	v_mul_f32_e32 v13, v13, v14
	v_med3_f32 v2, v2, s62, v196
	v_med3_f32 v3, v3, s62, v196
	v_med3_f32 v14, v8, s62, v196
	v_mov_b32_e32 v8, v169
	v_med3_f32 v15, v9, s62, v196
	v_cvt_pk_fp8_f32 v8, v2, v3
	v_med3_f32 v2, v10, s62, v196
	v_med3_f32 v3, v11, s62, v196
	v_mov_b32_e32 v9, v169
	v_cvt_pk_fp8_f32 v9, v2, v3
	v_ashrrev_i32_e32 v7, 31, v6
	v_med3_f32 v2, v12, s62, v196
	v_med3_f32 v3, v13, s62, v196
	v_cvt_pk_fp8_f32 v9, v2, v3 op_sel:[0,0,1]
	v_lshlrev_b64 v[2:3], 9, v[6:7]
	v_mul_f32_e32 v7, 0xbcb8aa3b, v142
	v_exp_f32_e32 v7, v7
	v_mul_f32_e32 v11, 0xbcb8aa3b, v143
	v_exp_f32_e32 v11, v11
	v_mul_f32_e32 v10, v142, v138
	v_add_f32_e32 v7, 1.0, v7
	v_rcp_f32_e32 v7, v7
	v_add_f32_e32 v11, 1.0, v11
	v_rcp_f32_e32 v11, v11
	v_mul_f32_e32 v10, 0x3a800000, v10
	v_mul_f32_e32 v7, v10, v7
	v_mul_f32_e32 v10, v143, v139
	v_mul_f32_e32 v10, 0x3a800000, v10
	v_mul_f32_e32 v10, v10, v11
	v_mul_f32_e32 v11, 0xbcb8aa3b, v144
	v_exp_f32_e32 v11, v11
	v_mul_f32_e32 v13, 0xbcb8aa3b, v145
	v_exp_f32_e32 v13, v13
	v_mul_f32_e32 v12, v144, v140
	v_add_f32_e32 v11, 1.0, v11
	v_rcp_f32_e32 v11, v11
	v_add_f32_e32 v13, 1.0, v13
	v_rcp_f32_e32 v13, v13
	v_mul_f32_e32 v12, 0x3a800000, v12
	v_mul_f32_e32 v11, v12, v11
	v_mul_f32_e32 v12, v145, v141
	v_mul_f32_e32 v12, 0x3a800000, v12
	v_mul_f32_e32 v12, v12, v13
	v_mul_f32_e32 v13, 0xbcb8aa3b, v134
	v_exp_f32_e32 v13, v13
	v_cvt_pk_fp8_f32 v8, v14, v15 op_sel:[0,0,1]
	v_mul_f32_e32 v15, 0xbcb8aa3b, v135
	v_exp_f32_e32 v15, v15
	v_add_f32_e32 v13, 1.0, v13
	v_rcp_f32_e32 v13, v13
	v_mul_f32_e32 v14, v134, v130
	v_add_f32_e32 v15, 1.0, v15
	v_rcp_f32_e32 v15, v15
	v_mul_f32_e32 v14, 0x3a800000, v14
	v_mul_f32_e32 v13, v14, v13
	v_mul_f32_e32 v14, v135, v131
	v_mul_f32_e32 v14, 0x3a800000, v14
	v_mul_f32_e32 v14, v14, v15
	v_mul_f32_e32 v15, 0xbcb8aa3b, v136
	v_exp_f32_e32 v15, v15
	v_mul_f32_e32 v17, 0xbcb8aa3b, v137
	v_exp_f32_e32 v17, v17
	v_mul_f32_e32 v16, v136, v132
	v_add_f32_e32 v15, 1.0, v15
	v_rcp_f32_e32 v15, v15
	v_add_f32_e32 v17, 1.0, v17
	v_rcp_f32_e32 v17, v17
	v_mul_f32_e32 v16, 0x3a800000, v16
	v_mul_f32_e32 v15, v16, v15
	v_mul_f32_e32 v16, v137, v133
	v_mul_f32_e32 v16, 0x3a800000, v16
	v_mul_f32_e32 v16, v16, v17
	v_med3_f32 v7, v7, s62, v196
	v_med3_f32 v17, v10, s62, v196
	v_mov_b32_e32 v10, v169
	v_med3_f32 v18, v11, s62, v196
	v_cvt_pk_fp8_f32 v10, v7, v17
	v_med3_f32 v7, v13, s62, v196
	v_med3_f32 v13, v14, s62, v196
	v_mov_b32_e32 v11, v169
	v_lshl_or_b32 v4, s26, 7, v190
	v_cvt_pk_fp8_f32 v11, v7, v13
	v_ashrrev_i32_e32 v5, 31, v4
	v_lshl_add_u64 v[2:3], s[12:13], 0, v[2:3]
	v_lshl_add_u64 v[2:3], v[2:3], 0, v[4:5]
	v_med3_f32 v12, v12, s62, v196
	global_store_dwordx2 v[2:3], v[8:9], off
	v_or_b32_e32 v8, 16, v6
	v_cvt_pk_fp8_f32 v10, v18, v12 op_sel:[0,0,1]
	v_med3_f32 v7, v15, s62, v196
	v_med3_f32 v12, v16, s62, v196
	v_ashrrev_i32_e32 v9, 31, v8
	v_cvt_pk_fp8_f32 v11, v7, v12 op_sel:[0,0,1]
	v_lshlrev_b64 v[8:9], 9, v[8:9]
	v_lshl_add_u64 v[8:9], s[12:13], 0, v[8:9]
	v_mul_f32_e32 v7, 0xbcb8aa3b, v126
	v_lshl_add_u64 v[8:9], v[8:9], 0, v[4:5]
	v_exp_f32_e32 v7, v7
	global_store_dwordx2 v[8:9], v[10:11], off
	v_mul_f32_e32 v11, 0xbcb8aa3b, v127
	v_exp_f32_e32 v11, v11
	v_add_f32_e32 v7, 1.0, v7
	v_rcp_f32_e32 v7, v7
	v_mul_f32_e32 v10, v126, v122
	v_add_f32_e32 v11, 1.0, v11
	v_rcp_f32_e32 v11, v11
	v_mul_f32_e32 v10, 0x3a800000, v10
	v_mul_f32_e32 v7, v10, v7
	v_mul_f32_e32 v10, v127, v123
	v_mul_f32_e32 v10, 0x3a800000, v10
	v_mul_f32_e32 v10, v10, v11
	v_mul_f32_e32 v11, 0xbcb8aa3b, v128
	v_exp_f32_e32 v11, v11
	v_mul_f32_e32 v13, 0xbcb8aa3b, v129
	v_exp_f32_e32 v13, v13
	v_mul_f32_e32 v12, v128, v124
	v_add_f32_e32 v11, 1.0, v11
	v_rcp_f32_e32 v11, v11
	v_add_f32_e32 v13, 1.0, v13
	v_rcp_f32_e32 v13, v13
	v_mul_f32_e32 v12, 0x3a800000, v12
	v_mul_f32_e32 v11, v12, v11
	v_mul_f32_e32 v12, v129, v125
	v_mul_f32_e32 v12, 0x3a800000, v12
	v_mul_f32_e32 v12, v12, v13
	v_mul_f32_e32 v13, 0xbcb8aa3b, v118
	v_exp_f32_e32 v13, v13
	v_mul_f32_e32 v15, 0xbcb8aa3b, v119
	v_exp_f32_e32 v15, v15
	v_mul_f32_e32 v14, v118, v114
	v_add_f32_e32 v13, 1.0, v13
	v_rcp_f32_e32 v13, v13
	v_add_f32_e32 v15, 1.0, v15
	v_rcp_f32_e32 v15, v15
	v_mul_f32_e32 v14, 0x3a800000, v14
	v_mul_f32_e32 v13, v14, v13
	v_mul_f32_e32 v14, v119, v115
	v_mul_f32_e32 v14, 0x3a800000, v14
	v_mul_f32_e32 v14, v14, v15
	v_mul_f32_e32 v15, 0xbcb8aa3b, v120
	v_exp_f32_e32 v15, v15
	v_mul_f32_e32 v17, 0xbcb8aa3b, v121
	v_exp_f32_e32 v17, v17
	v_mul_f32_e32 v16, v120, v116
	v_add_f32_e32 v15, 1.0, v15
	v_rcp_f32_e32 v15, v15
	v_add_f32_e32 v17, 1.0, v17
	v_rcp_f32_e32 v17, v17
	v_mul_f32_e32 v16, 0x3a800000, v16
	v_mul_f32_e32 v15, v16, v15
	v_mul_f32_e32 v16, v121, v117
	v_mul_f32_e32 v16, 0x3a800000, v16
	v_mul_f32_e32 v16, v16, v17
	v_med3_f32 v7, v7, s62, v196
	v_med3_f32 v17, v10, s62, v196
	v_mov_b32_e32 v10, v169
	v_med3_f32 v18, v11, s62, v196
	v_cvt_pk_fp8_f32 v10, v7, v17
	v_med3_f32 v7, v13, s62, v196
	v_med3_f32 v13, v14, s62, v196
	v_mov_b32_e32 v11, v169
	v_cvt_pk_fp8_f32 v11, v7, v13
	v_med3_f32 v12, v12, s62, v196
	v_or_b32_e32 v8, 32, v6
	v_cvt_pk_fp8_f32 v10, v18, v12 op_sel:[0,0,1]
	v_med3_f32 v7, v15, s62, v196
	v_med3_f32 v12, v16, s62, v196
	v_ashrrev_i32_e32 v9, 31, v8
	v_cvt_pk_fp8_f32 v11, v7, v12 op_sel:[0,0,1]
	v_lshlrev_b64 v[8:9], 9, v[8:9]
	v_lshl_add_u64 v[8:9], s[12:13], 0, v[8:9]
	v_lshl_add_u64 v[8:9], v[8:9], 0, v[4:5]
	global_store_dwordx2 v[8:9], v[10:11], off
	v_mul_f32_e32 v8, 0xbcb8aa3b, v110
	v_exp_f32_e32 v8, v8
	v_mul_f32_e32 v10, 0xbcb8aa3b, v111
	v_exp_f32_e32 v10, v10
	v_mul_f32_e32 v9, v110, v106
	v_add_f32_e32 v8, 1.0, v8
	v_rcp_f32_e32 v8, v8
	v_add_f32_e32 v10, 1.0, v10
	v_rcp_f32_e32 v10, v10
	v_mul_f32_e32 v9, 0x3a800000, v9
	v_mul_f32_e32 v8, v9, v8
	v_mul_f32_e32 v9, v111, v107
	v_mul_f32_e32 v9, 0x3a800000, v9
	v_mul_f32_e32 v9, v9, v10
	v_mul_f32_e32 v10, 0xbcb8aa3b, v112
	v_exp_f32_e32 v10, v10
	v_mul_f32_e32 v12, 0xbcb8aa3b, v113
	v_exp_f32_e32 v12, v12
	v_mul_f32_e32 v11, v112, v108
	v_add_f32_e32 v10, 1.0, v10
	v_rcp_f32_e32 v10, v10
	v_add_f32_e32 v12, 1.0, v12
	v_rcp_f32_e32 v12, v12
	v_mul_f32_e32 v11, 0x3a800000, v11
	v_mul_f32_e32 v10, v11, v10
	v_mul_f32_e32 v11, v113, v109
	v_mul_f32_e32 v11, 0x3a800000, v11
	v_mul_f32_e32 v11, v11, v12
	v_mul_f32_e32 v12, 0xbcb8aa3b, v102
	v_exp_f32_e32 v12, v12
	v_mul_f32_e32 v14, 0xbcb8aa3b, v103
	v_exp_f32_e32 v14, v14
	v_mul_f32_e32 v13, v102, v98
	v_add_f32_e32 v12, 1.0, v12
	v_rcp_f32_e32 v12, v12
	v_add_f32_e32 v14, 1.0, v14
	v_rcp_f32_e32 v14, v14
	v_mul_f32_e32 v13, 0x3a800000, v13
	v_mul_f32_e32 v12, v13, v12
	v_mul_f32_e32 v13, v103, v99
	v_mul_f32_e32 v13, 0x3a800000, v13
	v_mul_f32_e32 v13, v13, v14
	v_mul_f32_e32 v14, 0xbcb8aa3b, v104
	v_exp_f32_e32 v14, v14
	v_mul_f32_e32 v16, 0xbcb8aa3b, v105
	v_exp_f32_e32 v16, v16
	v_mul_f32_e32 v15, v104, v100
	v_add_f32_e32 v14, 1.0, v14
	v_rcp_f32_e32 v14, v14
	v_add_f32_e32 v16, 1.0, v16
	v_rcp_f32_e32 v16, v16
	v_mul_f32_e32 v15, 0x3a800000, v15
	v_mul_f32_e32 v14, v15, v14
	v_mul_f32_e32 v15, v105, v101
	v_mul_f32_e32 v15, 0x3a800000, v15
	v_mul_f32_e32 v15, v15, v16
	v_med3_f32 v16, v8, s62, v196
	v_med3_f32 v9, v9, s62, v196
	v_mov_b32_e32 v8, v169
	v_cvt_pk_fp8_f32 v8, v16, v9
	v_med3_f32 v12, v12, s62, v196
	v_med3_f32 v13, v13, s62, v196
	v_mov_b32_e32 v9, v169
	v_cvt_pk_fp8_f32 v9, v12, v13
	v_med3_f32 v10, v10, s62, v196
	v_med3_f32 v11, v11, s62, v196
	v_or_b32_e32 v6, 48, v6
	v_cvt_pk_fp8_f32 v8, v10, v11 op_sel:[0,0,1]
	v_med3_f32 v10, v14, s62, v196
	v_med3_f32 v11, v15, s62, v196
	v_ashrrev_i32_e32 v7, 31, v6
	v_cvt_pk_fp8_f32 v9, v10, v11 op_sel:[0,0,1]
	v_lshlrev_b64 v[6:7], 9, v[6:7]
	v_lshl_add_u64 v[6:7], s[12:13], 0, v[6:7]
	v_lshl_add_u64 v[4:5], v[6:7], 0, v[4:5]
	global_store_dwordx2 v[4:5], v[8:9], off
	v_mul_f32_e32 v4, 0xbcb8aa3b, v94
	v_exp_f32_e32 v4, v4
	v_mul_f32_e32 v6, 0xbcb8aa3b, v95
	v_exp_f32_e32 v6, v6
	v_mul_f32_e32 v5, v94, v90
	v_add_f32_e32 v4, 1.0, v4
	v_rcp_f32_e32 v4, v4
	v_add_f32_e32 v6, 1.0, v6
	v_rcp_f32_e32 v6, v6
	v_mul_f32_e32 v5, 0x3a800000, v5
	v_mul_f32_e32 v4, v5, v4
	v_mul_f32_e32 v5, v95, v91
	v_mul_f32_e32 v5, 0x3a800000, v5
	v_mul_f32_e32 v5, v5, v6
	v_mul_f32_e32 v6, 0xbcb8aa3b, v96
	v_exp_f32_e32 v6, v6
	v_mul_f32_e32 v8, 0xbcb8aa3b, v97
	v_exp_f32_e32 v8, v8
	v_mul_f32_e32 v7, v96, v92
	v_add_f32_e32 v6, 1.0, v6
	v_rcp_f32_e32 v6, v6
	v_add_f32_e32 v8, 1.0, v8
	v_rcp_f32_e32 v8, v8
	v_mul_f32_e32 v7, 0x3a800000, v7
	v_mul_f32_e32 v6, v7, v6
	v_mul_f32_e32 v7, v97, v93
	v_mul_f32_e32 v7, 0x3a800000, v7
	v_mul_f32_e32 v7, v7, v8
	v_mul_f32_e32 v8, 0xbcb8aa3b, v86
	v_exp_f32_e32 v8, v8
	v_mul_f32_e32 v10, 0xbcb8aa3b, v87
	v_exp_f32_e32 v10, v10
	v_mul_f32_e32 v9, v86, v82
	v_add_f32_e32 v8, 1.0, v8
	v_rcp_f32_e32 v8, v8
	v_add_f32_e32 v10, 1.0, v10
	v_rcp_f32_e32 v10, v10
	v_mul_f32_e32 v9, 0x3a800000, v9
	v_mul_f32_e32 v8, v9, v8
	v_mul_f32_e32 v9, v87, v83
	v_mul_f32_e32 v9, 0x3a800000, v9
	v_mul_f32_e32 v9, v9, v10
	v_mul_f32_e32 v10, 0xbcb8aa3b, v88
	v_exp_f32_e32 v10, v10
	v_mul_f32_e32 v12, 0xbcb8aa3b, v89
	v_exp_f32_e32 v12, v12
	v_mul_f32_e32 v11, v88, v84
	v_add_f32_e32 v10, 1.0, v10
	v_rcp_f32_e32 v10, v10
	v_add_f32_e32 v12, 1.0, v12
	v_rcp_f32_e32 v12, v12
	v_mul_f32_e32 v11, 0x3a800000, v11
	v_mul_f32_e32 v10, v11, v10
	v_mul_f32_e32 v11, v89, v85
	v_mul_f32_e32 v11, 0x3a800000, v11
	v_mul_f32_e32 v11, v11, v12
	v_med3_f32 v12, v4, s62, v196
	v_med3_f32 v5, v5, s62, v196
	v_mov_b32_e32 v4, v169
	v_cvt_pk_fp8_f32 v4, v12, v5
	v_med3_f32 v8, v8, s62, v196
	v_med3_f32 v9, v9, s62, v196
	v_mov_b32_e32 v5, v169
	v_cvt_pk_fp8_f32 v5, v8, v9
	v_med3_f32 v6, v6, s62, v196
	v_med3_f32 v7, v7, s62, v196
	v_cvt_pk_fp8_f32 v4, v6, v7 op_sel:[0,0,1]
	v_med3_f32 v6, v10, s62, v196
	v_med3_f32 v7, v11, s62, v196
	v_cvt_pk_fp8_f32 v5, v6, v7 op_sel:[0,0,1]
	v_add_co_u32_e32 v6, vcc, s49, v2
	v_mul_f32_e32 v8, 0xbcb8aa3b, v81
	s_nop 0
	v_addc_co_u32_e32 v7, vcc, 0, v3, vcc
	global_store_dwordx2 v[6:7], v[4:5], off
	v_mul_f32_e32 v4, 0xbcb8aa3b, v78
	v_exp_f32_e32 v4, v4
	v_mul_f32_e32 v6, 0xbcb8aa3b, v79
	v_exp_f32_e32 v6, v6
	v_mul_f32_e32 v5, v78, v74
	v_add_f32_e32 v4, 1.0, v4
	v_rcp_f32_e32 v4, v4
	v_add_f32_e32 v6, 1.0, v6
	v_rcp_f32_e32 v6, v6
	v_mul_f32_e32 v5, 0x3a800000, v5
	v_mul_f32_e32 v4, v5, v4
	v_mul_f32_e32 v5, v79, v75
	v_mul_f32_e32 v5, 0x3a800000, v5
	v_mul_f32_e32 v5, v5, v6
	v_mul_f32_e32 v6, 0xbcb8aa3b, v80
	v_exp_f32_e32 v6, v6
	v_exp_f32_e32 v8, v8
	v_mul_f32_e32 v7, v80, v76
	v_mul_f32_e32 v7, 0x3a800000, v7
	v_add_f32_e32 v6, 1.0, v6
	v_rcp_f32_e32 v6, v6
	v_add_f32_e32 v8, 1.0, v8
	v_rcp_f32_e32 v8, v8
	v_mul_f32_e32 v10, 0xbcb8aa3b, v71
	v_mul_f32_e32 v6, v7, v6
	v_mul_f32_e32 v7, v81, v77
	v_mul_f32_e32 v7, 0x3a800000, v7
	v_mul_f32_e32 v7, v7, v8
	v_mul_f32_e32 v8, 0xbcb8aa3b, v70
	v_exp_f32_e32 v8, v8
	v_exp_f32_e32 v10, v10
	v_mul_f32_e32 v9, v70, v66
	v_mul_f32_e32 v9, 0x3a800000, v9
	v_add_f32_e32 v8, 1.0, v8
	v_rcp_f32_e32 v8, v8
	v_add_f32_e32 v10, 1.0, v10
	v_rcp_f32_e32 v10, v10
	v_mul_f32_e32 v12, 0xbcb8aa3b, v73
	v_mul_f32_e32 v8, v9, v8
	v_mul_f32_e32 v9, v71, v67
	v_mul_f32_e32 v9, 0x3a800000, v9
	v_mul_f32_e32 v9, v9, v10
	v_mul_f32_e32 v10, 0xbcb8aa3b, v72
	v_exp_f32_e32 v10, v10
	v_exp_f32_e32 v12, v12
	v_mul_f32_e32 v11, v72, v68
	v_mul_f32_e32 v11, 0x3a800000, v11
	v_add_f32_e32 v10, 1.0, v10
	v_rcp_f32_e32 v10, v10
	v_add_f32_e32 v12, 1.0, v12
	v_rcp_f32_e32 v12, v12
	v_med3_f32 v5, v5, s62, v196
	v_mul_f32_e32 v10, v11, v10
	v_mul_f32_e32 v11, v73, v69
	v_mul_f32_e32 v11, 0x3a800000, v11
	v_mul_f32_e32 v11, v11, v12
	v_med3_f32 v12, v4, s62, v196
	v_mov_b32_e32 v4, v169
	v_cvt_pk_fp8_f32 v4, v12, v5
	v_med3_f32 v8, v8, s62, v196
	v_med3_f32 v9, v9, s62, v196
	v_mov_b32_e32 v5, v169
	v_cvt_pk_fp8_f32 v5, v8, v9
	v_med3_f32 v6, v6, s62, v196
	v_med3_f32 v7, v7, s62, v196
	v_cvt_pk_fp8_f32 v4, v6, v7 op_sel:[0,0,1]
	v_med3_f32 v6, v10, s62, v196
	v_med3_f32 v7, v11, s62, v196
	v_cvt_pk_fp8_f32 v5, v6, v7 op_sel:[0,0,1]
	v_add_co_u32_e32 v6, vcc, s50, v2
	v_mul_f32_e32 v8, 0xbcb8aa3b, v65
	s_nop 0
	v_addc_co_u32_e32 v7, vcc, 0, v3, vcc
	global_store_dwordx2 v[6:7], v[4:5], off
	v_mul_f32_e32 v4, 0xbcb8aa3b, v62
	v_exp_f32_e32 v4, v4
	v_mul_f32_e32 v6, 0xbcb8aa3b, v63
	v_exp_f32_e32 v6, v6
	v_mul_f32_e32 v5, v62, v58
	v_add_f32_e32 v4, 1.0, v4
	v_rcp_f32_e32 v4, v4
	v_add_f32_e32 v6, 1.0, v6
	v_rcp_f32_e32 v6, v6
	v_mul_f32_e32 v5, 0x3a800000, v5
	v_mul_f32_e32 v4, v5, v4
	v_mul_f32_e32 v5, v63, v59
	v_mul_f32_e32 v5, 0x3a800000, v5
	v_mul_f32_e32 v5, v5, v6
	v_mul_f32_e32 v6, 0xbcb8aa3b, v64
	v_exp_f32_e32 v6, v6
	v_exp_f32_e32 v8, v8
	v_mul_f32_e32 v7, v64, v60
	v_mul_f32_e32 v7, 0x3a800000, v7
	v_add_f32_e32 v6, 1.0, v6
	v_rcp_f32_e32 v6, v6
	v_add_f32_e32 v8, 1.0, v8
	v_rcp_f32_e32 v8, v8
	v_mul_f32_e32 v10, 0xbcb8aa3b, v55
	v_mul_f32_e32 v6, v7, v6
	v_mul_f32_e32 v7, v65, v61
	v_mul_f32_e32 v7, 0x3a800000, v7
	v_mul_f32_e32 v7, v7, v8
	v_mul_f32_e32 v8, 0xbcb8aa3b, v54
	v_exp_f32_e32 v8, v8
	v_exp_f32_e32 v10, v10
	v_mul_f32_e32 v9, v54, v50
	v_mul_f32_e32 v9, 0x3a800000, v9
	v_add_f32_e32 v8, 1.0, v8
	v_rcp_f32_e32 v8, v8
	v_add_f32_e32 v10, 1.0, v10
	v_rcp_f32_e32 v10, v10
	v_mul_f32_e32 v12, 0xbcb8aa3b, v57
	v_mul_f32_e32 v8, v9, v8
	v_mul_f32_e32 v9, v55, v51
	v_mul_f32_e32 v9, 0x3a800000, v9
	v_mul_f32_e32 v9, v9, v10
	v_mul_f32_e32 v10, 0xbcb8aa3b, v56
	v_exp_f32_e32 v10, v10
	v_exp_f32_e32 v12, v12
	v_mul_f32_e32 v11, v56, v52
	v_mul_f32_e32 v11, 0x3a800000, v11
	v_add_f32_e32 v10, 1.0, v10
	v_rcp_f32_e32 v10, v10
	v_add_f32_e32 v12, 1.0, v12
	v_rcp_f32_e32 v12, v12
	v_med3_f32 v5, v5, s62, v196
	v_mul_f32_e32 v10, v11, v10
	v_mul_f32_e32 v11, v57, v53
	v_mul_f32_e32 v11, 0x3a800000, v11
	v_mul_f32_e32 v11, v11, v12
	v_med3_f32 v12, v4, s62, v196
	v_mov_b32_e32 v4, v169
	v_cvt_pk_fp8_f32 v4, v12, v5
	v_med3_f32 v8, v8, s62, v196
	v_med3_f32 v9, v9, s62, v196
	v_mov_b32_e32 v5, v169
	v_cvt_pk_fp8_f32 v5, v8, v9
	v_med3_f32 v6, v6, s62, v196
	v_med3_f32 v7, v7, s62, v196
	v_cvt_pk_fp8_f32 v4, v6, v7 op_sel:[0,0,1]
	v_med3_f32 v6, v10, s62, v196
	v_med3_f32 v7, v11, s62, v196
	v_cvt_pk_fp8_f32 v5, v6, v7 op_sel:[0,0,1]
	v_add_co_u32_e32 v6, vcc, s51, v2
	v_mul_f32_e32 v8, 0xbcb8aa3b, v49
	s_nop 0
	v_addc_co_u32_e32 v7, vcc, 0, v3, vcc
	global_store_dwordx2 v[6:7], v[4:5], off
	v_mul_f32_e32 v4, 0xbcb8aa3b, v46
	v_exp_f32_e32 v4, v4
	v_mul_f32_e32 v6, 0xbcb8aa3b, v47
	v_exp_f32_e32 v6, v6
	v_mul_f32_e32 v5, v46, v42
	v_add_f32_e32 v4, 1.0, v4
	v_rcp_f32_e32 v4, v4
	v_add_f32_e32 v6, 1.0, v6
	v_rcp_f32_e32 v6, v6
	v_mul_f32_e32 v5, 0x3a800000, v5
	v_mul_f32_e32 v4, v5, v4
	v_mul_f32_e32 v5, v47, v43
	v_mul_f32_e32 v5, 0x3a800000, v5
	v_mul_f32_e32 v5, v5, v6
	v_mul_f32_e32 v6, 0xbcb8aa3b, v48
	v_exp_f32_e32 v6, v6
	v_exp_f32_e32 v8, v8
	v_mul_f32_e32 v7, v48, v44
	v_mul_f32_e32 v7, 0x3a800000, v7
	v_add_f32_e32 v6, 1.0, v6
	v_rcp_f32_e32 v6, v6
	v_add_f32_e32 v8, 1.0, v8
	v_rcp_f32_e32 v8, v8
	v_mul_f32_e32 v10, 0xbcb8aa3b, v39
	v_mul_f32_e32 v6, v7, v6
	v_mul_f32_e32 v7, v49, v45
	v_mul_f32_e32 v7, 0x3a800000, v7
	v_mul_f32_e32 v7, v7, v8
	v_mul_f32_e32 v8, 0xbcb8aa3b, v38
	v_exp_f32_e32 v8, v8
	v_exp_f32_e32 v10, v10
	v_mul_f32_e32 v9, v38, v34
	v_mul_f32_e32 v9, 0x3a800000, v9
	v_add_f32_e32 v8, 1.0, v8
	v_rcp_f32_e32 v8, v8
	v_add_f32_e32 v10, 1.0, v10
	v_rcp_f32_e32 v10, v10
	v_mul_f32_e32 v12, 0xbcb8aa3b, v41
	v_mul_f32_e32 v8, v9, v8
	v_mul_f32_e32 v9, v39, v35
	v_mul_f32_e32 v9, 0x3a800000, v9
	v_mul_f32_e32 v9, v9, v10
	v_mul_f32_e32 v10, 0xbcb8aa3b, v40
	v_exp_f32_e32 v10, v10
	v_exp_f32_e32 v12, v12
	v_mul_f32_e32 v11, v40, v36
	v_mul_f32_e32 v11, 0x3a800000, v11
	v_add_f32_e32 v10, 1.0, v10
	v_rcp_f32_e32 v10, v10
	v_add_f32_e32 v12, 1.0, v12
	v_rcp_f32_e32 v12, v12
	v_med3_f32 v5, v5, s62, v196
	v_mul_f32_e32 v10, v11, v10
	v_mul_f32_e32 v11, v41, v37
	v_mul_f32_e32 v11, 0x3a800000, v11
	v_mul_f32_e32 v11, v11, v12
	v_med3_f32 v12, v4, s62, v196
	v_mov_b32_e32 v4, v169
	v_cvt_pk_fp8_f32 v4, v12, v5
	v_med3_f32 v8, v8, s62, v196
	v_med3_f32 v9, v9, s62, v196
	v_mov_b32_e32 v5, v169
	v_cvt_pk_fp8_f32 v5, v8, v9
	v_med3_f32 v6, v6, s62, v196
	v_med3_f32 v7, v7, s62, v196
	v_cvt_pk_fp8_f32 v4, v6, v7 op_sel:[0,0,1]
	v_med3_f32 v6, v10, s62, v196
	v_med3_f32 v7, v11, s62, v196
	v_cvt_pk_fp8_f32 v5, v6, v7 op_sel:[0,0,1]
	v_add_co_u32_e32 v2, vcc, 0x16000, v2
	s_nop 1
	v_addc_co_u32_e32 v3, vcc, 0, v3, vcc
	s_and_b64 vcc, exec, s[2:3]
	s_mov_b64 s[2:3], -1
	global_store_dwordx2 v[2:3], v[4:5], off
	s_mov_b32 s101, 1
	s_cbranch_vccnz .LBB0_1357
	s_andn2_b64 vcc, exec, s[10:11]
	s_cbranch_vccnz .LBB0_1356
	s_barrier
	s_branch .LBB0_1356
